# v10 + hand-pipelined adaLN GEMV k-loop (13 row loads in flight) + q/k gain loads hoisted out of the head-norm row loop
# speedup vs baseline: 1.0012x; 1.0012x over previous
; __device__ __forceinline__ float sigmoidf_(float x) { return __builtin_amdgcn_rcpf(1.0f + __builtin_amdgcn_exp2f(-1.4426950408889634f * x)); }
; #define GAS __attribute__((address_space(1)))
; __device__ __forceinline__ void gemv_item(Frame& F, int item) {
;     const int nb = item % 96, ks = item / 96, n0 = nb * 256 + 4 * F.lane, k0 = ks * 64;
;     float cs[4];
; #pragma unroll
;     for (int b = 0; b < 4; ++b) { const float cv = F.c[b * DM + k0 + F.lane]; cs[b] = cv * pg8::sigmoidf_(cv); }
;     f32x4 acc[4];
; #pragma unroll
;     for (int b = 0; b < 4; ++b) acc[b] = (f32x4){0.f, 0.f, 0.f, 0.f};
;     const float* wp = F.ada_w + (size_t)k0 * MODW + n0;
; #pragma unroll 16
;     for (int k = 0; k < 64; ++k) { const f32x4 w = __builtin_nontemporal_load((const GAS f32x4*)(wp + (size_t)k * MODW));
; #pragma unroll
;         for (int b = 0; b < 4; ++b) { const float s = __builtin_bit_cast(float, __builtin_amdgcn_readlane(__builtin_bit_cast(int, cs[b]), k)); acc[b] += w * s; } }
.LBB0_10:
	s_mul_hi_i32 s0, s39, 0x2aaaaaab
	s_lshr_b32 s1, s0, 31
	s_ashr_i32 s41, s0, 4
	s_add_i32 s41, s41, s1
	s_lshl_b32 s0, s41, 6
	v_or_b32_e32 v2, s0, v180
	v_readlane_b32 s4, v249, 15
	v_ashrrev_i32_e32 v3, 31, v2
	v_readlane_b32 s6, v249, 17
	v_readlane_b32 s7, v249, 18
	v_add_u32_e32 v6, 0x2000, v2
	v_ashrrev_i32_e32 v7, 31, v6
	v_lshl_add_u64 v[4:5], v[2:3], 2, s[6:7]
	global_load_dword v13, v[4:5], off
	v_add_u32_e32 v4, 0x1000, v2
	v_add_u32_e32 v2, 0x3000, v2
	v_ashrrev_i32_e32 v5, 31, v4
	v_ashrrev_i32_e32 v3, 31, v2
	v_lshl_add_u64 v[4:5], v[4:5], 2, s[6:7]
	v_lshl_add_u64 v[2:3], v[2:3], 2, s[6:7]
	v_lshl_add_u64 v[6:7], v[6:7], 2, s[6:7]
	global_load_dword v4, v[4:5], off
	s_nop 0
	global_load_dword v5, v[6:7], off
	s_nop 0
	global_load_dword v2, v[2:3], off
	s_mul_i32 s1, s41, 0x60
	s_mul_i32 s2, s41, 0x600000
	s_sub_i32 s1, s39, s1
	s_mul_hi_i32 s3, s0, 0x18000
	v_lshl_or_b32 v38, s1, 8, v1
	s_add_u32 s0, s35, s2
	v_mov_b32_e32 v6, 0
	v_ashrrev_i32_e32 v39, 31, v38
	s_addc_u32 s1, s37, s3
	v_readlane_b32 s86, v249, 46
	s_mov_b32 s43, 0
	v_mov_b32_e32 v7, v6
	v_mov_b32_e32 v8, v6
	v_mov_b32_e32 v9, v6
	v_mov_b32_e32 v18, v6
	v_mov_b32_e32 v19, v6
	v_mov_b32_e32 v20, v6
	v_mov_b32_e32 v21, v6
	v_mov_b32_e32 v14, v6
	v_mov_b32_e32 v15, v6
	v_mov_b32_e32 v16, v6
	v_mov_b32_e32 v17, v6
	v_mov_b32_e32 v10, v6
	v_mov_b32_e32 v11, v6
	v_mov_b32_e32 v12, v6
	v_lshl_add_u64 v[40:41], v[38:39], 2, s[0:1]
	v_readlane_b32 s87, v249, 47
	v_readlane_b32 s5, v249, 16
	v_readlane_b32 s8, v249, 19
	v_readlane_b32 s9, v249, 20
	v_readlane_b32 s10, v249, 21
	v_readlane_b32 s11, v249, 22
	v_readlane_b32 s12, v249, 23
	v_readlane_b32 s13, v249, 24
	v_readlane_b32 s14, v249, 25
	v_readlane_b32 s15, v249, 26
	v_readlane_b32 s16, v249, 27
	v_readlane_b32 s17, v249, 28
	v_readlane_b32 s18, v249, 29
	v_readlane_b32 s19, v249, 30
	s_waitcnt vmcnt(3)
	v_mul_f32_e32 v3, 0xbfb8aa3b, v13
	v_exp_f32_e32 v3, v3
	s_waitcnt vmcnt(2)
	v_mul_f32_e32 v22, 0xbfb8aa3b, v4
	s_waitcnt vmcnt(1)
	v_mul_f32_e32 v23, 0xbfb8aa3b, v5
	s_waitcnt vmcnt(0)
	v_mul_f32_e32 v24, 0xbfb8aa3b, v2
	v_exp_f32_e32 v22, v22
	v_exp_f32_e32 v23, v23
	v_exp_f32_e32 v24, v24
	v_add_f32_e32 v3, 1.0, v3
	v_add_f32_e32 v22, 1.0, v22
	v_add_f32_e32 v23, 1.0, v23
	v_add_f32_e32 v24, 1.0, v24
	v_rcp_f32_e32 v3, v3
	v_rcp_f32_e32 v22, v22
	v_rcp_f32_e32 v23, v23
	v_rcp_f32_e32 v24, v24
	v_mul_f32_e32 v58, v13, v3
	v_mul_f32_e32 v59, v4, v22
	v_mul_f32_e32 v60, v5, v23
	v_mul_f32_e32 v61, v2, v24
	v_mov_b32_e32 v13, v6
	s_add_u32 s18, s0, 0xfff40000
	s_addc_u32 s19, s1, -1
	v_lshlrev_b32_e32 v78, 2, v38
	global_load_dwordx4 v[2:5], v78, s[18:19] nt
	s_add_u32 s18, s18, 0x18000
	s_addc_u32 s19, s19, 0
	global_load_dwordx4 v[22:25], v78, s[18:19] nt
	s_add_u32 s18, s18, 0x18000
	s_addc_u32 s19, s19, 0
	global_load_dwordx4 v[26:29], v78, s[18:19] nt
	s_add_u32 s18, s18, 0x18000
	s_addc_u32 s19, s19, 0
	global_load_dwordx4 v[30:33], v78, s[18:19] nt
	s_add_u32 s18, s18, 0x18000
	s_addc_u32 s19, s19, 0
	global_load_dwordx4 v[34:37], v78, s[18:19] nt
	s_add_u32 s18, s18, 0x18000
	s_addc_u32 s19, s19, 0
	global_load_dwordx4 v[40:43], v78, s[18:19] nt
	s_add_u32 s18, s18, 0x18000
	s_addc_u32 s19, s19, 0
	global_load_dwordx4 v[44:47], v78, s[18:19] nt
	s_add_u32 s18, s18, 0x18000
	s_addc_u32 s19, s19, 0
	global_load_dwordx4 v[48:51], v78, s[18:19] nt
	s_add_u32 s18, s18, 0x18000
	s_addc_u32 s19, s19, 0
	global_load_dwordx4 v[52:55], v78, s[18:19] nt
	s_add_u32 s18, s18, 0x18000
	s_addc_u32 s19, s19, 0
	global_load_dwordx4 v[62:65], v78, s[18:19] nt
	s_add_u32 s18, s18, 0x18000
	s_addc_u32 s19, s19, 0
	global_load_dwordx4 v[66:69], v78, s[18:19] nt
	s_add_u32 s18, s18, 0x18000
	s_addc_u32 s19, s19, 0
	global_load_dwordx4 v[70:73], v78, s[18:19] nt
	s_add_u32 s18, s18, 0x18000
	s_addc_u32 s19, s19, 0
	global_load_dwordx4 v[74:77], v78, s[18:19] nt
	s_add_u32 s18, s18, 0x18000
	s_addc_u32 s19, s19, 0
	v_readlane_b32 s2, v58, 0
	v_readlane_b32 s4, v59, 0
	v_readlane_b32 s6, v60, 0
	v_readlane_b32 s8, v61, 0
	s_waitcnt vmcnt(12)
	v_readlane_b32 s10, v58, 1
	v_readlane_b32 s12, v59, 1
	v_readlane_b32 s14, v60, 1
	v_readlane_b32 s16, v61, 1
	v_pk_fma_f32 v[18:19], v[2:3], s[2:3], v[18:19] op_sel_hi:[1,0,1]
	v_pk_fma_f32 v[20:21], v[4:5], s[2:3], v[20:21] op_sel_hi:[1,0,1]
	v_pk_fma_f32 v[14:15], v[2:3], s[4:5], v[14:15] op_sel_hi:[1,0,1]
	v_pk_fma_f32 v[16:17], v[4:5], s[4:5], v[16:17] op_sel_hi:[1,0,1]
	v_pk_fma_f32 v[10:11], v[2:3], s[6:7], v[10:11] op_sel_hi:[1,0,1]
	v_pk_fma_f32 v[12:13], v[4:5], s[6:7], v[12:13] op_sel_hi:[1,0,1]
	v_pk_fma_f32 v[6:7], v[2:3], s[8:9], v[6:7] op_sel_hi:[1,0,1]
	v_pk_fma_f32 v[8:9], v[4:5], s[8:9], v[8:9] op_sel_hi:[1,0,1]
	global_load_dwordx4 v[2:5], v78, s[18:19] nt
	s_add_u32 s18, s18, 0x18000
	s_addc_u32 s19, s19, 0
	s_waitcnt vmcnt(12)
	v_readlane_b32 s2, v58, 2
	v_readlane_b32 s4, v59, 2
	v_readlane_b32 s6, v60, 2
	v_readlane_b32 s8, v61, 2
	v_pk_fma_f32 v[18:19], v[22:23], s[10:11], v[18:19] op_sel_hi:[1,0,1]
	v_pk_fma_f32 v[20:21], v[24:25], s[10:11], v[20:21] op_sel_hi:[1,0,1]
	v_pk_fma_f32 v[14:15], v[22:23], s[12:13], v[14:15] op_sel_hi:[1,0,1]
	v_pk_fma_f32 v[16:17], v[24:25], s[12:13], v[16:17] op_sel_hi:[1,0,1]
	v_pk_fma_f32 v[10:11], v[22:23], s[14:15], v[10:11] op_sel_hi:[1,0,1]
	v_pk_fma_f32 v[12:13], v[24:25], s[14:15], v[12:13] op_sel_hi:[1,0,1]
	v_pk_fma_f32 v[6:7], v[22:23], s[16:17], v[6:7] op_sel_hi:[1,0,1]
	v_pk_fma_f32 v[8:9], v[24:25], s[16:17], v[8:9] op_sel_hi:[1,0,1]
	global_load_dwordx4 v[22:25], v78, s[18:19] nt
	s_add_u32 s18, s18, 0x18000
	s_addc_u32 s19, s19, 0
	s_waitcnt vmcnt(12)
; #define GAS __attribute__((address_space(1)))
; __device__ __forceinline__ void gemv_item(Frame& F, int item) {
;     ...
; #pragma unroll 16
;     for (int k = 0; k < 64; ++k) { const f32x4 w = __builtin_nontemporal_load((const GAS f32x4*)(wp + (size_t)k * MODW));
; #pragma unroll
;         for (int b = 0; b < 4; ++b) { const float s = __builtin_bit_cast(float, __builtin_amdgcn_readlane(__builtin_bit_cast(int, cs[b]), k)); acc[b] += w * s; } }
	v_readlane_b32 s10, v58, 3
	v_readlane_b32 s12, v59, 3
	v_readlane_b32 s14, v60, 3
	v_readlane_b32 s16, v61, 3
	v_pk_fma_f32 v[18:19], v[26:27], s[2:3], v[18:19] op_sel_hi:[1,0,1]
	v_pk_fma_f32 v[20:21], v[28:29], s[2:3], v[20:21] op_sel_hi:[1,0,1]
	v_pk_fma_f32 v[14:15], v[26:27], s[4:5], v[14:15] op_sel_hi:[1,0,1]
	v_pk_fma_f32 v[16:17], v[28:29], s[4:5], v[16:17] op_sel_hi:[1,0,1]
	v_pk_fma_f32 v[10:11], v[26:27], s[6:7], v[10:11] op_sel_hi:[1,0,1]
	v_pk_fma_f32 v[12:13], v[28:29], s[6:7], v[12:13] op_sel_hi:[1,0,1]
	v_pk_fma_f32 v[6:7], v[26:27], s[8:9], v[6:7] op_sel_hi:[1,0,1]
	v_pk_fma_f32 v[8:9], v[28:29], s[8:9], v[8:9] op_sel_hi:[1,0,1]
	global_load_dwordx4 v[26:29], v78, s[18:19] nt
	s_add_u32 s18, s18, 0x18000
	s_addc_u32 s19, s19, 0
	s_waitcnt vmcnt(12)
	v_readlane_b32 s2, v58, 4
	v_readlane_b32 s4, v59, 4
	v_readlane_b32 s6, v60, 4
	v_readlane_b32 s8, v61, 4
	v_pk_fma_f32 v[18:19], v[30:31], s[10:11], v[18:19] op_sel_hi:[1,0,1]
	v_pk_fma_f32 v[20:21], v[32:33], s[10:11], v[20:21] op_sel_hi:[1,0,1]
	v_pk_fma_f32 v[14:15], v[30:31], s[12:13], v[14:15] op_sel_hi:[1,0,1]
	v_pk_fma_f32 v[16:17], v[32:33], s[12:13], v[16:17] op_sel_hi:[1,0,1]
	v_pk_fma_f32 v[10:11], v[30:31], s[14:15], v[10:11] op_sel_hi:[1,0,1]
	v_pk_fma_f32 v[12:13], v[32:33], s[14:15], v[12:13] op_sel_hi:[1,0,1]
	v_pk_fma_f32 v[6:7], v[30:31], s[16:17], v[6:7] op_sel_hi:[1,0,1]
	v_pk_fma_f32 v[8:9], v[32:33], s[16:17], v[8:9] op_sel_hi:[1,0,1]
	global_load_dwordx4 v[30:33], v78, s[18:19] nt
	s_add_u32 s18, s18, 0x18000
	s_addc_u32 s19, s19, 0
	s_waitcnt vmcnt(12)
	v_readlane_b32 s10, v58, 5
	v_readlane_b32 s12, v59, 5
	v_readlane_b32 s14, v60, 5
	v_readlane_b32 s16, v61, 5
	v_pk_fma_f32 v[18:19], v[34:35], s[2:3], v[18:19] op_sel_hi:[1,0,1]
	v_pk_fma_f32 v[20:21], v[36:37], s[2:3], v[20:21] op_sel_hi:[1,0,1]
	v_pk_fma_f32 v[14:15], v[34:35], s[4:5], v[14:15] op_sel_hi:[1,0,1]
	v_pk_fma_f32 v[16:17], v[36:37], s[4:5], v[16:17] op_sel_hi:[1,0,1]
	v_pk_fma_f32 v[10:11], v[34:35], s[6:7], v[10:11] op_sel_hi:[1,0,1]
	v_pk_fma_f32 v[12:13], v[36:37], s[6:7], v[12:13] op_sel_hi:[1,0,1]
	v_pk_fma_f32 v[6:7], v[34:35], s[8:9], v[6:7] op_sel_hi:[1,0,1]
	v_pk_fma_f32 v[8:9], v[36:37], s[8:9], v[8:9] op_sel_hi:[1,0,1]
	global_load_dwordx4 v[34:37], v78, s[18:19] nt
	s_add_u32 s18, s18, 0x18000
	s_addc_u32 s19, s19, 0
	s_waitcnt vmcnt(12)
	v_readlane_b32 s2, v58, 6
	v_readlane_b32 s4, v59, 6
	v_readlane_b32 s6, v60, 6
	v_readlane_b32 s8, v61, 6
	v_pk_fma_f32 v[18:19], v[40:41], s[10:11], v[18:19] op_sel_hi:[1,0,1]
	v_pk_fma_f32 v[20:21], v[42:43], s[10:11], v[20:21] op_sel_hi:[1,0,1]
	v_pk_fma_f32 v[14:15], v[40:41], s[12:13], v[14:15] op_sel_hi:[1,0,1]
	v_pk_fma_f32 v[16:17], v[42:43], s[12:13], v[16:17] op_sel_hi:[1,0,1]
	v_pk_fma_f32 v[10:11], v[40:41], s[14:15], v[10:11] op_sel_hi:[1,0,1]
	v_pk_fma_f32 v[12:13], v[42:43], s[14:15], v[12:13] op_sel_hi:[1,0,1]
	v_pk_fma_f32 v[6:7], v[40:41], s[16:17], v[6:7] op_sel_hi:[1,0,1]
	v_pk_fma_f32 v[8:9], v[42:43], s[16:17], v[8:9] op_sel_hi:[1,0,1]
	global_load_dwordx4 v[40:43], v78, s[18:19] nt
	s_add_u32 s18, s18, 0x18000
	s_addc_u32 s19, s19, 0
	s_waitcnt vmcnt(12)
	v_readlane_b32 s10, v58, 7
	v_readlane_b32 s12, v59, 7
	v_readlane_b32 s14, v60, 7
	v_readlane_b32 s16, v61, 7
	v_pk_fma_f32 v[18:19], v[44:45], s[2:3], v[18:19] op_sel_hi:[1,0,1]
	v_pk_fma_f32 v[20:21], v[46:47], s[2:3], v[20:21] op_sel_hi:[1,0,1]
	v_pk_fma_f32 v[14:15], v[44:45], s[4:5], v[14:15] op_sel_hi:[1,0,1]
	v_pk_fma_f32 v[16:17], v[46:47], s[4:5], v[16:17] op_sel_hi:[1,0,1]
	v_pk_fma_f32 v[10:11], v[44:45], s[6:7], v[10:11] op_sel_hi:[1,0,1]
	v_pk_fma_f32 v[12:13], v[46:47], s[6:7], v[12:13] op_sel_hi:[1,0,1]
	v_pk_fma_f32 v[6:7], v[44:45], s[8:9], v[6:7] op_sel_hi:[1,0,1]
	v_pk_fma_f32 v[8:9], v[46:47], s[8:9], v[8:9] op_sel_hi:[1,0,1]
	global_load_dwordx4 v[44:47], v78, s[18:19] nt
	s_add_u32 s18, s18, 0x18000
	s_addc_u32 s19, s19, 0
	s_waitcnt vmcnt(12)
	v_readlane_b32 s2, v58, 8
	v_readlane_b32 s4, v59, 8
	v_readlane_b32 s6, v60, 8
	v_readlane_b32 s8, v61, 8
	v_pk_fma_f32 v[18:19], v[48:49], s[10:11], v[18:19] op_sel_hi:[1,0,1]
	v_pk_fma_f32 v[20:21], v[50:51], s[10:11], v[20:21] op_sel_hi:[1,0,1]
	v_pk_fma_f32 v[14:15], v[48:49], s[12:13], v[14:15] op_sel_hi:[1,0,1]
	v_pk_fma_f32 v[16:17], v[50:51], s[12:13], v[16:17] op_sel_hi:[1,0,1]
	v_pk_fma_f32 v[10:11], v[48:49], s[14:15], v[10:11] op_sel_hi:[1,0,1]
	v_pk_fma_f32 v[12:13], v[50:51], s[14:15], v[12:13] op_sel_hi:[1,0,1]
	v_pk_fma_f32 v[6:7], v[48:49], s[16:17], v[6:7] op_sel_hi:[1,0,1]
	v_pk_fma_f32 v[8:9], v[50:51], s[16:17], v[8:9] op_sel_hi:[1,0,1]
	global_load_dwordx4 v[48:51], v78, s[18:19] nt
	s_add_u32 s18, s18, 0x18000
	s_addc_u32 s19, s19, 0
	s_waitcnt vmcnt(12)
	v_readlane_b32 s10, v58, 9
	v_readlane_b32 s12, v59, 9
	v_readlane_b32 s14, v60, 9
	v_readlane_b32 s16, v61, 9
	v_pk_fma_f32 v[18:19], v[52:53], s[2:3], v[18:19] op_sel_hi:[1,0,1]
	v_pk_fma_f32 v[20:21], v[54:55], s[2:3], v[20:21] op_sel_hi:[1,0,1]
	v_pk_fma_f32 v[14:15], v[52:53], s[4:5], v[14:15] op_sel_hi:[1,0,1]
	v_pk_fma_f32 v[16:17], v[54:55], s[4:5], v[16:17] op_sel_hi:[1,0,1]
	v_pk_fma_f32 v[10:11], v[52:53], s[6:7], v[10:11] op_sel_hi:[1,0,1]
	v_pk_fma_f32 v[12:13], v[54:55], s[6:7], v[12:13] op_sel_hi:[1,0,1]
	v_pk_fma_f32 v[6:7], v[52:53], s[8:9], v[6:7] op_sel_hi:[1,0,1]
	v_pk_fma_f32 v[8:9], v[54:55], s[8:9], v[8:9] op_sel_hi:[1,0,1]
	global_load_dwordx4 v[52:55], v78, s[18:19] nt
	s_add_u32 s18, s18, 0x18000
	s_addc_u32 s19, s19, 0
	s_waitcnt vmcnt(12)
; #define GAS __attribute__((address_space(1)))
; __device__ __forceinline__ void gemv_item(Frame& F, int item) {
;     ...
; #pragma unroll 16
;     for (int k = 0; k < 64; ++k) { const f32x4 w = __builtin_nontemporal_load((const GAS f32x4*)(wp + (size_t)k * MODW));
; #pragma unroll
;         for (int b = 0; b < 4; ++b) { const float s = __builtin_bit_cast(float, __builtin_amdgcn_readlane(__builtin_bit_cast(int, cs[b]), k)); acc[b] += w * s; } }
	v_readlane_b32 s2, v58, 10
	v_readlane_b32 s4, v59, 10
	v_readlane_b32 s6, v60, 10
	v_readlane_b32 s8, v61, 10
	v_pk_fma_f32 v[18:19], v[62:63], s[10:11], v[18:19] op_sel_hi:[1,0,1]
	v_pk_fma_f32 v[20:21], v[64:65], s[10:11], v[20:21] op_sel_hi:[1,0,1]
	v_pk_fma_f32 v[14:15], v[62:63], s[12:13], v[14:15] op_sel_hi:[1,0,1]
	v_pk_fma_f32 v[16:17], v[64:65], s[12:13], v[16:17] op_sel_hi:[1,0,1]
	v_pk_fma_f32 v[10:11], v[62:63], s[14:15], v[10:11] op_sel_hi:[1,0,1]
	v_pk_fma_f32 v[12:13], v[64:65], s[14:15], v[12:13] op_sel_hi:[1,0,1]
	v_pk_fma_f32 v[6:7], v[62:63], s[16:17], v[6:7] op_sel_hi:[1,0,1]
	v_pk_fma_f32 v[8:9], v[64:65], s[16:17], v[8:9] op_sel_hi:[1,0,1]
	global_load_dwordx4 v[62:65], v78, s[18:19] nt
	s_add_u32 s18, s18, 0x18000
	s_addc_u32 s19, s19, 0
	s_waitcnt vmcnt(12)
	v_readlane_b32 s10, v58, 11
	v_readlane_b32 s12, v59, 11
	v_readlane_b32 s14, v60, 11
	v_readlane_b32 s16, v61, 11
	v_pk_fma_f32 v[18:19], v[66:67], s[2:3], v[18:19] op_sel_hi:[1,0,1]
	v_pk_fma_f32 v[20:21], v[68:69], s[2:3], v[20:21] op_sel_hi:[1,0,1]
	v_pk_fma_f32 v[14:15], v[66:67], s[4:5], v[14:15] op_sel_hi:[1,0,1]
	v_pk_fma_f32 v[16:17], v[68:69], s[4:5], v[16:17] op_sel_hi:[1,0,1]
	v_pk_fma_f32 v[10:11], v[66:67], s[6:7], v[10:11] op_sel_hi:[1,0,1]
	v_pk_fma_f32 v[12:13], v[68:69], s[6:7], v[12:13] op_sel_hi:[1,0,1]
	v_pk_fma_f32 v[6:7], v[66:67], s[8:9], v[6:7] op_sel_hi:[1,0,1]
	v_pk_fma_f32 v[8:9], v[68:69], s[8:9], v[8:9] op_sel_hi:[1,0,1]
	global_load_dwordx4 v[66:69], v78, s[18:19] nt
	s_add_u32 s18, s18, 0x18000
	s_addc_u32 s19, s19, 0
	s_waitcnt vmcnt(12)
	v_readlane_b32 s2, v58, 12
	v_readlane_b32 s4, v59, 12
	v_readlane_b32 s6, v60, 12
	v_readlane_b32 s8, v61, 12
	v_pk_fma_f32 v[18:19], v[70:71], s[10:11], v[18:19] op_sel_hi:[1,0,1]
	v_pk_fma_f32 v[20:21], v[72:73], s[10:11], v[20:21] op_sel_hi:[1,0,1]
	v_pk_fma_f32 v[14:15], v[70:71], s[12:13], v[14:15] op_sel_hi:[1,0,1]
	v_pk_fma_f32 v[16:17], v[72:73], s[12:13], v[16:17] op_sel_hi:[1,0,1]
	v_pk_fma_f32 v[10:11], v[70:71], s[14:15], v[10:11] op_sel_hi:[1,0,1]
	v_pk_fma_f32 v[12:13], v[72:73], s[14:15], v[12:13] op_sel_hi:[1,0,1]
	v_pk_fma_f32 v[6:7], v[70:71], s[16:17], v[6:7] op_sel_hi:[1,0,1]
	v_pk_fma_f32 v[8:9], v[72:73], s[16:17], v[8:9] op_sel_hi:[1,0,1]
	global_load_dwordx4 v[70:73], v78, s[18:19] nt
	s_add_u32 s18, s18, 0x18000
	s_addc_u32 s19, s19, 0
	s_waitcnt vmcnt(12)
	v_readlane_b32 s10, v58, 13
	v_readlane_b32 s12, v59, 13
	v_readlane_b32 s14, v60, 13
	v_readlane_b32 s16, v61, 13
	v_pk_fma_f32 v[18:19], v[74:75], s[2:3], v[18:19] op_sel_hi:[1,0,1]
	v_pk_fma_f32 v[20:21], v[76:77], s[2:3], v[20:21] op_sel_hi:[1,0,1]
	v_pk_fma_f32 v[14:15], v[74:75], s[4:5], v[14:15] op_sel_hi:[1,0,1]
	v_pk_fma_f32 v[16:17], v[76:77], s[4:5], v[16:17] op_sel_hi:[1,0,1]
	v_pk_fma_f32 v[10:11], v[74:75], s[6:7], v[10:11] op_sel_hi:[1,0,1]
	v_pk_fma_f32 v[12:13], v[76:77], s[6:7], v[12:13] op_sel_hi:[1,0,1]
	v_pk_fma_f32 v[6:7], v[74:75], s[8:9], v[6:7] op_sel_hi:[1,0,1]
	v_pk_fma_f32 v[8:9], v[76:77], s[8:9], v[8:9] op_sel_hi:[1,0,1]
	global_load_dwordx4 v[74:77], v78, s[18:19] nt
	s_add_u32 s18, s18, 0x18000
	s_addc_u32 s19, s19, 0
	s_waitcnt vmcnt(12)
	v_readlane_b32 s2, v58, 14
	v_readlane_b32 s4, v59, 14
	v_readlane_b32 s6, v60, 14
	v_readlane_b32 s8, v61, 14
	v_pk_fma_f32 v[18:19], v[2:3], s[10:11], v[18:19] op_sel_hi:[1,0,1]
	v_pk_fma_f32 v[20:21], v[4:5], s[10:11], v[20:21] op_sel_hi:[1,0,1]
	v_pk_fma_f32 v[14:15], v[2:3], s[12:13], v[14:15] op_sel_hi:[1,0,1]
	v_pk_fma_f32 v[16:17], v[4:5], s[12:13], v[16:17] op_sel_hi:[1,0,1]
	v_pk_fma_f32 v[10:11], v[2:3], s[14:15], v[10:11] op_sel_hi:[1,0,1]
	v_pk_fma_f32 v[12:13], v[4:5], s[14:15], v[12:13] op_sel_hi:[1,0,1]
	v_pk_fma_f32 v[6:7], v[2:3], s[16:17], v[6:7] op_sel_hi:[1,0,1]
	v_pk_fma_f32 v[8:9], v[4:5], s[16:17], v[8:9] op_sel_hi:[1,0,1]
	global_load_dwordx4 v[2:5], v78, s[18:19] nt
	s_add_u32 s18, s18, 0x18000
	s_addc_u32 s19, s19, 0
	s_waitcnt vmcnt(12)
	v_readlane_b32 s10, v58, 15
	v_readlane_b32 s12, v59, 15
	v_readlane_b32 s14, v60, 15
	v_readlane_b32 s16, v61, 15
	v_pk_fma_f32 v[18:19], v[22:23], s[2:3], v[18:19] op_sel_hi:[1,0,1]
	v_pk_fma_f32 v[20:21], v[24:25], s[2:3], v[20:21] op_sel_hi:[1,0,1]
	v_pk_fma_f32 v[14:15], v[22:23], s[4:5], v[14:15] op_sel_hi:[1,0,1]
	v_pk_fma_f32 v[16:17], v[24:25], s[4:5], v[16:17] op_sel_hi:[1,0,1]
	v_pk_fma_f32 v[10:11], v[22:23], s[6:7], v[10:11] op_sel_hi:[1,0,1]
	v_pk_fma_f32 v[12:13], v[24:25], s[6:7], v[12:13] op_sel_hi:[1,0,1]
	v_pk_fma_f32 v[6:7], v[22:23], s[8:9], v[6:7] op_sel_hi:[1,0,1]
	v_pk_fma_f32 v[8:9], v[24:25], s[8:9], v[8:9] op_sel_hi:[1,0,1]
	global_load_dwordx4 v[22:25], v78, s[18:19] nt
	s_add_u32 s18, s18, 0x18000
	s_addc_u32 s19, s19, 0
	s_waitcnt vmcnt(12)
	v_readlane_b32 s2, v58, 16
	v_readlane_b32 s4, v59, 16
	v_readlane_b32 s6, v60, 16
	v_readlane_b32 s8, v61, 16
	v_pk_fma_f32 v[18:19], v[26:27], s[10:11], v[18:19] op_sel_hi:[1,0,1]
	v_pk_fma_f32 v[20:21], v[28:29], s[10:11], v[20:21] op_sel_hi:[1,0,1]
	v_pk_fma_f32 v[14:15], v[26:27], s[12:13], v[14:15] op_sel_hi:[1,0,1]
	v_pk_fma_f32 v[16:17], v[28:29], s[12:13], v[16:17] op_sel_hi:[1,0,1]
	v_pk_fma_f32 v[10:11], v[26:27], s[14:15], v[10:11] op_sel_hi:[1,0,1]
	v_pk_fma_f32 v[12:13], v[28:29], s[14:15], v[12:13] op_sel_hi:[1,0,1]
	v_pk_fma_f32 v[6:7], v[26:27], s[16:17], v[6:7] op_sel_hi:[1,0,1]
	v_pk_fma_f32 v[8:9], v[28:29], s[16:17], v[8:9] op_sel_hi:[1,0,1]
	global_load_dwordx4 v[26:29], v78, s[18:19] nt
	s_add_u32 s18, s18, 0x18000
	s_addc_u32 s19, s19, 0
	s_waitcnt vmcnt(12)
; #define GAS __attribute__((address_space(1)))
; __device__ __forceinline__ void gemv_item(Frame& F, int item) {
;     ...
; #pragma unroll 16
;     for (int k = 0; k < 64; ++k) { const f32x4 w = __builtin_nontemporal_load((const GAS f32x4*)(wp + (size_t)k * MODW));
; #pragma unroll
;         for (int b = 0; b < 4; ++b) { const float s = __builtin_bit_cast(float, __builtin_amdgcn_readlane(__builtin_bit_cast(int, cs[b]), k)); acc[b] += w * s; } }
	v_readlane_b32 s10, v58, 17
	v_readlane_b32 s12, v59, 17
	v_readlane_b32 s14, v60, 17
	v_readlane_b32 s16, v61, 17
	v_pk_fma_f32 v[18:19], v[30:31], s[2:3], v[18:19] op_sel_hi:[1,0,1]
	v_pk_fma_f32 v[20:21], v[32:33], s[2:3], v[20:21] op_sel_hi:[1,0,1]
	v_pk_fma_f32 v[14:15], v[30:31], s[4:5], v[14:15] op_sel_hi:[1,0,1]
	v_pk_fma_f32 v[16:17], v[32:33], s[4:5], v[16:17] op_sel_hi:[1,0,1]
	v_pk_fma_f32 v[10:11], v[30:31], s[6:7], v[10:11] op_sel_hi:[1,0,1]
	v_pk_fma_f32 v[12:13], v[32:33], s[6:7], v[12:13] op_sel_hi:[1,0,1]
	v_pk_fma_f32 v[6:7], v[30:31], s[8:9], v[6:7] op_sel_hi:[1,0,1]
	v_pk_fma_f32 v[8:9], v[32:33], s[8:9], v[8:9] op_sel_hi:[1,0,1]
	global_load_dwordx4 v[30:33], v78, s[18:19] nt
	s_add_u32 s18, s18, 0x18000
	s_addc_u32 s19, s19, 0
	s_waitcnt vmcnt(12)
	v_readlane_b32 s2, v58, 18
	v_readlane_b32 s4, v59, 18
	v_readlane_b32 s6, v60, 18
	v_readlane_b32 s8, v61, 18
	v_pk_fma_f32 v[18:19], v[34:35], s[10:11], v[18:19] op_sel_hi:[1,0,1]
	v_pk_fma_f32 v[20:21], v[36:37], s[10:11], v[20:21] op_sel_hi:[1,0,1]
	v_pk_fma_f32 v[14:15], v[34:35], s[12:13], v[14:15] op_sel_hi:[1,0,1]
	v_pk_fma_f32 v[16:17], v[36:37], s[12:13], v[16:17] op_sel_hi:[1,0,1]
	v_pk_fma_f32 v[10:11], v[34:35], s[14:15], v[10:11] op_sel_hi:[1,0,1]
	v_pk_fma_f32 v[12:13], v[36:37], s[14:15], v[12:13] op_sel_hi:[1,0,1]
	v_pk_fma_f32 v[6:7], v[34:35], s[16:17], v[6:7] op_sel_hi:[1,0,1]
	v_pk_fma_f32 v[8:9], v[36:37], s[16:17], v[8:9] op_sel_hi:[1,0,1]
	global_load_dwordx4 v[34:37], v78, s[18:19] nt
	s_add_u32 s18, s18, 0x18000
	s_addc_u32 s19, s19, 0
	s_waitcnt vmcnt(12)
	v_readlane_b32 s10, v58, 19
	v_readlane_b32 s12, v59, 19
	v_readlane_b32 s14, v60, 19
	v_readlane_b32 s16, v61, 19
	v_pk_fma_f32 v[18:19], v[40:41], s[2:3], v[18:19] op_sel_hi:[1,0,1]
	v_pk_fma_f32 v[20:21], v[42:43], s[2:3], v[20:21] op_sel_hi:[1,0,1]
	v_pk_fma_f32 v[14:15], v[40:41], s[4:5], v[14:15] op_sel_hi:[1,0,1]
	v_pk_fma_f32 v[16:17], v[42:43], s[4:5], v[16:17] op_sel_hi:[1,0,1]
	v_pk_fma_f32 v[10:11], v[40:41], s[6:7], v[10:11] op_sel_hi:[1,0,1]
	v_pk_fma_f32 v[12:13], v[42:43], s[6:7], v[12:13] op_sel_hi:[1,0,1]
	v_pk_fma_f32 v[6:7], v[40:41], s[8:9], v[6:7] op_sel_hi:[1,0,1]
	v_pk_fma_f32 v[8:9], v[42:43], s[8:9], v[8:9] op_sel_hi:[1,0,1]
	global_load_dwordx4 v[40:43], v78, s[18:19] nt
	s_add_u32 s18, s18, 0x18000
	s_addc_u32 s19, s19, 0
	s_waitcnt vmcnt(12)
	v_readlane_b32 s2, v58, 20
	v_readlane_b32 s4, v59, 20
	v_readlane_b32 s6, v60, 20
	v_readlane_b32 s8, v61, 20
	v_pk_fma_f32 v[18:19], v[44:45], s[10:11], v[18:19] op_sel_hi:[1,0,1]
	v_pk_fma_f32 v[20:21], v[46:47], s[10:11], v[20:21] op_sel_hi:[1,0,1]
	v_pk_fma_f32 v[14:15], v[44:45], s[12:13], v[14:15] op_sel_hi:[1,0,1]
	v_pk_fma_f32 v[16:17], v[46:47], s[12:13], v[16:17] op_sel_hi:[1,0,1]
	v_pk_fma_f32 v[10:11], v[44:45], s[14:15], v[10:11] op_sel_hi:[1,0,1]
	v_pk_fma_f32 v[12:13], v[46:47], s[14:15], v[12:13] op_sel_hi:[1,0,1]
	v_pk_fma_f32 v[6:7], v[44:45], s[16:17], v[6:7] op_sel_hi:[1,0,1]
	v_pk_fma_f32 v[8:9], v[46:47], s[16:17], v[8:9] op_sel_hi:[1,0,1]
	global_load_dwordx4 v[44:47], v78, s[18:19] nt
	s_add_u32 s18, s18, 0x18000
	s_addc_u32 s19, s19, 0
	s_waitcnt vmcnt(12)
	v_readlane_b32 s10, v58, 21
	v_readlane_b32 s12, v59, 21
	v_readlane_b32 s14, v60, 21
	v_readlane_b32 s16, v61, 21
	v_pk_fma_f32 v[18:19], v[48:49], s[2:3], v[18:19] op_sel_hi:[1,0,1]
	v_pk_fma_f32 v[20:21], v[50:51], s[2:3], v[20:21] op_sel_hi:[1,0,1]
	v_pk_fma_f32 v[14:15], v[48:49], s[4:5], v[14:15] op_sel_hi:[1,0,1]
	v_pk_fma_f32 v[16:17], v[50:51], s[4:5], v[16:17] op_sel_hi:[1,0,1]
	v_pk_fma_f32 v[10:11], v[48:49], s[6:7], v[10:11] op_sel_hi:[1,0,1]
	v_pk_fma_f32 v[12:13], v[50:51], s[6:7], v[12:13] op_sel_hi:[1,0,1]
	v_pk_fma_f32 v[6:7], v[48:49], s[8:9], v[6:7] op_sel_hi:[1,0,1]
	v_pk_fma_f32 v[8:9], v[50:51], s[8:9], v[8:9] op_sel_hi:[1,0,1]
	global_load_dwordx4 v[48:51], v78, s[18:19] nt
	s_add_u32 s18, s18, 0x18000
	s_addc_u32 s19, s19, 0
	s_waitcnt vmcnt(12)
	v_readlane_b32 s2, v58, 22
	v_readlane_b32 s4, v59, 22
	v_readlane_b32 s6, v60, 22
	v_readlane_b32 s8, v61, 22
	v_pk_fma_f32 v[18:19], v[52:53], s[10:11], v[18:19] op_sel_hi:[1,0,1]
	v_pk_fma_f32 v[20:21], v[54:55], s[10:11], v[20:21] op_sel_hi:[1,0,1]
	v_pk_fma_f32 v[14:15], v[52:53], s[12:13], v[14:15] op_sel_hi:[1,0,1]
	v_pk_fma_f32 v[16:17], v[54:55], s[12:13], v[16:17] op_sel_hi:[1,0,1]
	v_pk_fma_f32 v[10:11], v[52:53], s[14:15], v[10:11] op_sel_hi:[1,0,1]
	v_pk_fma_f32 v[12:13], v[54:55], s[14:15], v[12:13] op_sel_hi:[1,0,1]
	v_pk_fma_f32 v[6:7], v[52:53], s[16:17], v[6:7] op_sel_hi:[1,0,1]
	v_pk_fma_f32 v[8:9], v[54:55], s[16:17], v[8:9] op_sel_hi:[1,0,1]
	global_load_dwordx4 v[52:55], v78, s[18:19] nt
	s_add_u32 s18, s18, 0x18000
	s_addc_u32 s19, s19, 0
	s_waitcnt vmcnt(12)
	v_readlane_b32 s10, v58, 23
	v_readlane_b32 s12, v59, 23
	v_readlane_b32 s14, v60, 23
	v_readlane_b32 s16, v61, 23
	v_pk_fma_f32 v[18:19], v[62:63], s[2:3], v[18:19] op_sel_hi:[1,0,1]
	v_pk_fma_f32 v[20:21], v[64:65], s[2:3], v[20:21] op_sel_hi:[1,0,1]
	v_pk_fma_f32 v[14:15], v[62:63], s[4:5], v[14:15] op_sel_hi:[1,0,1]
	v_pk_fma_f32 v[16:17], v[64:65], s[4:5], v[16:17] op_sel_hi:[1,0,1]
	v_pk_fma_f32 v[10:11], v[62:63], s[6:7], v[10:11] op_sel_hi:[1,0,1]
	v_pk_fma_f32 v[12:13], v[64:65], s[6:7], v[12:13] op_sel_hi:[1,0,1]
	v_pk_fma_f32 v[6:7], v[62:63], s[8:9], v[6:7] op_sel_hi:[1,0,1]
	v_pk_fma_f32 v[8:9], v[64:65], s[8:9], v[8:9] op_sel_hi:[1,0,1]
	global_load_dwordx4 v[62:65], v78, s[18:19] nt
	s_add_u32 s18, s18, 0x18000
	s_addc_u32 s19, s19, 0
	s_waitcnt vmcnt(12)
; #define GAS __attribute__((address_space(1)))
; __device__ __forceinline__ void gemv_item(Frame& F, int item) {
;     ...
; #pragma unroll 16
;     for (int k = 0; k < 64; ++k) { const f32x4 w = __builtin_nontemporal_load((const GAS f32x4*)(wp + (size_t)k * MODW));
; #pragma unroll
;         for (int b = 0; b < 4; ++b) { const float s = __builtin_bit_cast(float, __builtin_amdgcn_readlane(__builtin_bit_cast(int, cs[b]), k)); acc[b] += w * s; } }
	v_readlane_b32 s2, v58, 24
	v_readlane_b32 s4, v59, 24
	v_readlane_b32 s6, v60, 24
	v_readlane_b32 s8, v61, 24
	v_pk_fma_f32 v[18:19], v[66:67], s[10:11], v[18:19] op_sel_hi:[1,0,1]
	v_pk_fma_f32 v[20:21], v[68:69], s[10:11], v[20:21] op_sel_hi:[1,0,1]
	v_pk_fma_f32 v[14:15], v[66:67], s[12:13], v[14:15] op_sel_hi:[1,0,1]
	v_pk_fma_f32 v[16:17], v[68:69], s[12:13], v[16:17] op_sel_hi:[1,0,1]
	v_pk_fma_f32 v[10:11], v[66:67], s[14:15], v[10:11] op_sel_hi:[1,0,1]
	v_pk_fma_f32 v[12:13], v[68:69], s[14:15], v[12:13] op_sel_hi:[1,0,1]
	v_pk_fma_f32 v[6:7], v[66:67], s[16:17], v[6:7] op_sel_hi:[1,0,1]
	v_pk_fma_f32 v[8:9], v[68:69], s[16:17], v[8:9] op_sel_hi:[1,0,1]
	global_load_dwordx4 v[66:69], v78, s[18:19] nt
	s_add_u32 s18, s18, 0x18000
	s_addc_u32 s19, s19, 0
	s_waitcnt vmcnt(12)
	v_readlane_b32 s10, v58, 25
	v_readlane_b32 s12, v59, 25
	v_readlane_b32 s14, v60, 25
	v_readlane_b32 s16, v61, 25
	v_pk_fma_f32 v[18:19], v[70:71], s[2:3], v[18:19] op_sel_hi:[1,0,1]
	v_pk_fma_f32 v[20:21], v[72:73], s[2:3], v[20:21] op_sel_hi:[1,0,1]
	v_pk_fma_f32 v[14:15], v[70:71], s[4:5], v[14:15] op_sel_hi:[1,0,1]
	v_pk_fma_f32 v[16:17], v[72:73], s[4:5], v[16:17] op_sel_hi:[1,0,1]
	v_pk_fma_f32 v[10:11], v[70:71], s[6:7], v[10:11] op_sel_hi:[1,0,1]
	v_pk_fma_f32 v[12:13], v[72:73], s[6:7], v[12:13] op_sel_hi:[1,0,1]
	v_pk_fma_f32 v[6:7], v[70:71], s[8:9], v[6:7] op_sel_hi:[1,0,1]
	v_pk_fma_f32 v[8:9], v[72:73], s[8:9], v[8:9] op_sel_hi:[1,0,1]
	global_load_dwordx4 v[70:73], v78, s[18:19] nt
	s_add_u32 s18, s18, 0x18000
	s_addc_u32 s19, s19, 0
	s_waitcnt vmcnt(12)
	v_readlane_b32 s2, v58, 26
	v_readlane_b32 s4, v59, 26
	v_readlane_b32 s6, v60, 26
	v_readlane_b32 s8, v61, 26
	v_pk_fma_f32 v[18:19], v[74:75], s[10:11], v[18:19] op_sel_hi:[1,0,1]
	v_pk_fma_f32 v[20:21], v[76:77], s[10:11], v[20:21] op_sel_hi:[1,0,1]
	v_pk_fma_f32 v[14:15], v[74:75], s[12:13], v[14:15] op_sel_hi:[1,0,1]
	v_pk_fma_f32 v[16:17], v[76:77], s[12:13], v[16:17] op_sel_hi:[1,0,1]
	v_pk_fma_f32 v[10:11], v[74:75], s[14:15], v[10:11] op_sel_hi:[1,0,1]
	v_pk_fma_f32 v[12:13], v[76:77], s[14:15], v[12:13] op_sel_hi:[1,0,1]
	v_pk_fma_f32 v[6:7], v[74:75], s[16:17], v[6:7] op_sel_hi:[1,0,1]
	v_pk_fma_f32 v[8:9], v[76:77], s[16:17], v[8:9] op_sel_hi:[1,0,1]
	global_load_dwordx4 v[74:77], v78, s[18:19] nt
	s_add_u32 s18, s18, 0x18000
	s_addc_u32 s19, s19, 0
	s_waitcnt vmcnt(12)
	v_readlane_b32 s10, v58, 27
	v_readlane_b32 s12, v59, 27
	v_readlane_b32 s14, v60, 27
	v_readlane_b32 s16, v61, 27
	v_pk_fma_f32 v[18:19], v[2:3], s[2:3], v[18:19] op_sel_hi:[1,0,1]
	v_pk_fma_f32 v[20:21], v[4:5], s[2:3], v[20:21] op_sel_hi:[1,0,1]
	v_pk_fma_f32 v[14:15], v[2:3], s[4:5], v[14:15] op_sel_hi:[1,0,1]
	v_pk_fma_f32 v[16:17], v[4:5], s[4:5], v[16:17] op_sel_hi:[1,0,1]
	v_pk_fma_f32 v[10:11], v[2:3], s[6:7], v[10:11] op_sel_hi:[1,0,1]
	v_pk_fma_f32 v[12:13], v[4:5], s[6:7], v[12:13] op_sel_hi:[1,0,1]
	v_pk_fma_f32 v[6:7], v[2:3], s[8:9], v[6:7] op_sel_hi:[1,0,1]
	v_pk_fma_f32 v[8:9], v[4:5], s[8:9], v[8:9] op_sel_hi:[1,0,1]
	global_load_dwordx4 v[2:5], v78, s[18:19] nt
	s_add_u32 s18, s18, 0x18000
	s_addc_u32 s19, s19, 0
	s_waitcnt vmcnt(12)
	v_readlane_b32 s2, v58, 28
	v_readlane_b32 s4, v59, 28
	v_readlane_b32 s6, v60, 28
	v_readlane_b32 s8, v61, 28
	v_pk_fma_f32 v[18:19], v[22:23], s[10:11], v[18:19] op_sel_hi:[1,0,1]
	v_pk_fma_f32 v[20:21], v[24:25], s[10:11], v[20:21] op_sel_hi:[1,0,1]
	v_pk_fma_f32 v[14:15], v[22:23], s[12:13], v[14:15] op_sel_hi:[1,0,1]
	v_pk_fma_f32 v[16:17], v[24:25], s[12:13], v[16:17] op_sel_hi:[1,0,1]
	v_pk_fma_f32 v[10:11], v[22:23], s[14:15], v[10:11] op_sel_hi:[1,0,1]
	v_pk_fma_f32 v[12:13], v[24:25], s[14:15], v[12:13] op_sel_hi:[1,0,1]
	v_pk_fma_f32 v[6:7], v[22:23], s[16:17], v[6:7] op_sel_hi:[1,0,1]
	v_pk_fma_f32 v[8:9], v[24:25], s[16:17], v[8:9] op_sel_hi:[1,0,1]
	global_load_dwordx4 v[22:25], v78, s[18:19] nt
	s_add_u32 s18, s18, 0x18000
	s_addc_u32 s19, s19, 0
	s_waitcnt vmcnt(12)
	v_readlane_b32 s10, v58, 29
	v_readlane_b32 s12, v59, 29
	v_readlane_b32 s14, v60, 29
	v_readlane_b32 s16, v61, 29
	v_pk_fma_f32 v[18:19], v[26:27], s[2:3], v[18:19] op_sel_hi:[1,0,1]
	v_pk_fma_f32 v[20:21], v[28:29], s[2:3], v[20:21] op_sel_hi:[1,0,1]
	v_pk_fma_f32 v[14:15], v[26:27], s[4:5], v[14:15] op_sel_hi:[1,0,1]
	v_pk_fma_f32 v[16:17], v[28:29], s[4:5], v[16:17] op_sel_hi:[1,0,1]
	v_pk_fma_f32 v[10:11], v[26:27], s[6:7], v[10:11] op_sel_hi:[1,0,1]
	v_pk_fma_f32 v[12:13], v[28:29], s[6:7], v[12:13] op_sel_hi:[1,0,1]
	v_pk_fma_f32 v[6:7], v[26:27], s[8:9], v[6:7] op_sel_hi:[1,0,1]
	v_pk_fma_f32 v[8:9], v[28:29], s[8:9], v[8:9] op_sel_hi:[1,0,1]
	global_load_dwordx4 v[26:29], v78, s[18:19] nt
	s_add_u32 s18, s18, 0x18000
	s_addc_u32 s19, s19, 0
	s_waitcnt vmcnt(12)
	v_readlane_b32 s2, v58, 30
	v_readlane_b32 s4, v59, 30
	v_readlane_b32 s6, v60, 30
	v_readlane_b32 s8, v61, 30
	v_pk_fma_f32 v[18:19], v[30:31], s[10:11], v[18:19] op_sel_hi:[1,0,1]
	v_pk_fma_f32 v[20:21], v[32:33], s[10:11], v[20:21] op_sel_hi:[1,0,1]
	v_pk_fma_f32 v[14:15], v[30:31], s[12:13], v[14:15] op_sel_hi:[1,0,1]
	v_pk_fma_f32 v[16:17], v[32:33], s[12:13], v[16:17] op_sel_hi:[1,0,1]
	v_pk_fma_f32 v[10:11], v[30:31], s[14:15], v[10:11] op_sel_hi:[1,0,1]
	v_pk_fma_f32 v[12:13], v[32:33], s[14:15], v[12:13] op_sel_hi:[1,0,1]
	v_pk_fma_f32 v[6:7], v[30:31], s[16:17], v[6:7] op_sel_hi:[1,0,1]
	v_pk_fma_f32 v[8:9], v[32:33], s[16:17], v[8:9] op_sel_hi:[1,0,1]
	global_load_dwordx4 v[30:33], v78, s[18:19] nt
	s_add_u32 s18, s18, 0x18000
	s_addc_u32 s19, s19, 0
	s_waitcnt vmcnt(12)
; #define GAS __attribute__((address_space(1)))
; __device__ __forceinline__ void gemv_item(Frame& F, int item) {
;     ...
; #pragma unroll 16
;     for (int k = 0; k < 64; ++k) { const f32x4 w = __builtin_nontemporal_load((const GAS f32x4*)(wp + (size_t)k * MODW));
; #pragma unroll
;         for (int b = 0; b < 4; ++b) { const float s = __builtin_bit_cast(float, __builtin_amdgcn_readlane(__builtin_bit_cast(int, cs[b]), k)); acc[b] += w * s; } }
	v_readlane_b32 s10, v58, 31
	v_readlane_b32 s12, v59, 31
	v_readlane_b32 s14, v60, 31
	v_readlane_b32 s16, v61, 31
	v_pk_fma_f32 v[18:19], v[34:35], s[2:3], v[18:19] op_sel_hi:[1,0,1]
	v_pk_fma_f32 v[20:21], v[36:37], s[2:3], v[20:21] op_sel_hi:[1,0,1]
	v_pk_fma_f32 v[14:15], v[34:35], s[4:5], v[14:15] op_sel_hi:[1,0,1]
	v_pk_fma_f32 v[16:17], v[36:37], s[4:5], v[16:17] op_sel_hi:[1,0,1]
	v_pk_fma_f32 v[10:11], v[34:35], s[6:7], v[10:11] op_sel_hi:[1,0,1]
	v_pk_fma_f32 v[12:13], v[36:37], s[6:7], v[12:13] op_sel_hi:[1,0,1]
	v_pk_fma_f32 v[6:7], v[34:35], s[8:9], v[6:7] op_sel_hi:[1,0,1]
	v_pk_fma_f32 v[8:9], v[36:37], s[8:9], v[8:9] op_sel_hi:[1,0,1]
	global_load_dwordx4 v[34:37], v78, s[18:19] nt
	s_add_u32 s18, s18, 0x18000
	s_addc_u32 s19, s19, 0
	s_waitcnt vmcnt(12)
	v_readlane_b32 s2, v58, 32
	v_readlane_b32 s4, v59, 32
	v_readlane_b32 s6, v60, 32
	v_readlane_b32 s8, v61, 32
	v_pk_fma_f32 v[18:19], v[40:41], s[10:11], v[18:19] op_sel_hi:[1,0,1]
	v_pk_fma_f32 v[20:21], v[42:43], s[10:11], v[20:21] op_sel_hi:[1,0,1]
	v_pk_fma_f32 v[14:15], v[40:41], s[12:13], v[14:15] op_sel_hi:[1,0,1]
	v_pk_fma_f32 v[16:17], v[42:43], s[12:13], v[16:17] op_sel_hi:[1,0,1]
	v_pk_fma_f32 v[10:11], v[40:41], s[14:15], v[10:11] op_sel_hi:[1,0,1]
	v_pk_fma_f32 v[12:13], v[42:43], s[14:15], v[12:13] op_sel_hi:[1,0,1]
	v_pk_fma_f32 v[6:7], v[40:41], s[16:17], v[6:7] op_sel_hi:[1,0,1]
	v_pk_fma_f32 v[8:9], v[42:43], s[16:17], v[8:9] op_sel_hi:[1,0,1]
	global_load_dwordx4 v[40:43], v78, s[18:19] nt
	s_add_u32 s18, s18, 0x18000
	s_addc_u32 s19, s19, 0
	s_waitcnt vmcnt(12)
	v_readlane_b32 s10, v58, 33
	v_readlane_b32 s12, v59, 33
	v_readlane_b32 s14, v60, 33
	v_readlane_b32 s16, v61, 33
	v_pk_fma_f32 v[18:19], v[44:45], s[2:3], v[18:19] op_sel_hi:[1,0,1]
	v_pk_fma_f32 v[20:21], v[46:47], s[2:3], v[20:21] op_sel_hi:[1,0,1]
	v_pk_fma_f32 v[14:15], v[44:45], s[4:5], v[14:15] op_sel_hi:[1,0,1]
	v_pk_fma_f32 v[16:17], v[46:47], s[4:5], v[16:17] op_sel_hi:[1,0,1]
	v_pk_fma_f32 v[10:11], v[44:45], s[6:7], v[10:11] op_sel_hi:[1,0,1]
	v_pk_fma_f32 v[12:13], v[46:47], s[6:7], v[12:13] op_sel_hi:[1,0,1]
	v_pk_fma_f32 v[6:7], v[44:45], s[8:9], v[6:7] op_sel_hi:[1,0,1]
	v_pk_fma_f32 v[8:9], v[46:47], s[8:9], v[8:9] op_sel_hi:[1,0,1]
	global_load_dwordx4 v[44:47], v78, s[18:19] nt
	s_add_u32 s18, s18, 0x18000
	s_addc_u32 s19, s19, 0
	s_waitcnt vmcnt(12)
	v_readlane_b32 s2, v58, 34
	v_readlane_b32 s4, v59, 34
	v_readlane_b32 s6, v60, 34
	v_readlane_b32 s8, v61, 34
	v_pk_fma_f32 v[18:19], v[48:49], s[10:11], v[18:19] op_sel_hi:[1,0,1]
	v_pk_fma_f32 v[20:21], v[50:51], s[10:11], v[20:21] op_sel_hi:[1,0,1]
	v_pk_fma_f32 v[14:15], v[48:49], s[12:13], v[14:15] op_sel_hi:[1,0,1]
	v_pk_fma_f32 v[16:17], v[50:51], s[12:13], v[16:17] op_sel_hi:[1,0,1]
	v_pk_fma_f32 v[10:11], v[48:49], s[14:15], v[10:11] op_sel_hi:[1,0,1]
	v_pk_fma_f32 v[12:13], v[50:51], s[14:15], v[12:13] op_sel_hi:[1,0,1]
	v_pk_fma_f32 v[6:7], v[48:49], s[16:17], v[6:7] op_sel_hi:[1,0,1]
	v_pk_fma_f32 v[8:9], v[50:51], s[16:17], v[8:9] op_sel_hi:[1,0,1]
	global_load_dwordx4 v[48:51], v78, s[18:19] nt
	s_add_u32 s18, s18, 0x18000
	s_addc_u32 s19, s19, 0
	s_waitcnt vmcnt(12)
	v_readlane_b32 s10, v58, 35
	v_readlane_b32 s12, v59, 35
	v_readlane_b32 s14, v60, 35
	v_readlane_b32 s16, v61, 35
	v_pk_fma_f32 v[18:19], v[52:53], s[2:3], v[18:19] op_sel_hi:[1,0,1]
	v_pk_fma_f32 v[20:21], v[54:55], s[2:3], v[20:21] op_sel_hi:[1,0,1]
	v_pk_fma_f32 v[14:15], v[52:53], s[4:5], v[14:15] op_sel_hi:[1,0,1]
	v_pk_fma_f32 v[16:17], v[54:55], s[4:5], v[16:17] op_sel_hi:[1,0,1]
	v_pk_fma_f32 v[10:11], v[52:53], s[6:7], v[10:11] op_sel_hi:[1,0,1]
	v_pk_fma_f32 v[12:13], v[54:55], s[6:7], v[12:13] op_sel_hi:[1,0,1]
	v_pk_fma_f32 v[6:7], v[52:53], s[8:9], v[6:7] op_sel_hi:[1,0,1]
	v_pk_fma_f32 v[8:9], v[54:55], s[8:9], v[8:9] op_sel_hi:[1,0,1]
	global_load_dwordx4 v[52:55], v78, s[18:19] nt
	s_add_u32 s18, s18, 0x18000
	s_addc_u32 s19, s19, 0
	s_waitcnt vmcnt(12)
	v_readlane_b32 s2, v58, 36
	v_readlane_b32 s4, v59, 36
	v_readlane_b32 s6, v60, 36
	v_readlane_b32 s8, v61, 36
	v_pk_fma_f32 v[18:19], v[62:63], s[10:11], v[18:19] op_sel_hi:[1,0,1]
	v_pk_fma_f32 v[20:21], v[64:65], s[10:11], v[20:21] op_sel_hi:[1,0,1]
	v_pk_fma_f32 v[14:15], v[62:63], s[12:13], v[14:15] op_sel_hi:[1,0,1]
	v_pk_fma_f32 v[16:17], v[64:65], s[12:13], v[16:17] op_sel_hi:[1,0,1]
	v_pk_fma_f32 v[10:11], v[62:63], s[14:15], v[10:11] op_sel_hi:[1,0,1]
	v_pk_fma_f32 v[12:13], v[64:65], s[14:15], v[12:13] op_sel_hi:[1,0,1]
	v_pk_fma_f32 v[6:7], v[62:63], s[16:17], v[6:7] op_sel_hi:[1,0,1]
	v_pk_fma_f32 v[8:9], v[64:65], s[16:17], v[8:9] op_sel_hi:[1,0,1]
	global_load_dwordx4 v[62:65], v78, s[18:19] nt
	s_add_u32 s18, s18, 0x18000
	s_addc_u32 s19, s19, 0
	s_waitcnt vmcnt(12)
	v_readlane_b32 s10, v58, 37
	v_readlane_b32 s12, v59, 37
	v_readlane_b32 s14, v60, 37
	v_readlane_b32 s16, v61, 37
	v_pk_fma_f32 v[18:19], v[66:67], s[2:3], v[18:19] op_sel_hi:[1,0,1]
	v_pk_fma_f32 v[20:21], v[68:69], s[2:3], v[20:21] op_sel_hi:[1,0,1]
	v_pk_fma_f32 v[14:15], v[66:67], s[4:5], v[14:15] op_sel_hi:[1,0,1]
	v_pk_fma_f32 v[16:17], v[68:69], s[4:5], v[16:17] op_sel_hi:[1,0,1]
	v_pk_fma_f32 v[10:11], v[66:67], s[6:7], v[10:11] op_sel_hi:[1,0,1]
	v_pk_fma_f32 v[12:13], v[68:69], s[6:7], v[12:13] op_sel_hi:[1,0,1]
	v_pk_fma_f32 v[6:7], v[66:67], s[8:9], v[6:7] op_sel_hi:[1,0,1]
	v_pk_fma_f32 v[8:9], v[68:69], s[8:9], v[8:9] op_sel_hi:[1,0,1]
	global_load_dwordx4 v[66:69], v78, s[18:19] nt
	s_add_u32 s18, s18, 0x18000
	s_addc_u32 s19, s19, 0
	s_waitcnt vmcnt(12)
; #define GAS __attribute__((address_space(1)))
; __device__ __forceinline__ void gemv_item(Frame& F, int item) {
;     ...
; #pragma unroll 16
;     for (int k = 0; k < 64; ++k) { const f32x4 w = __builtin_nontemporal_load((const GAS f32x4*)(wp + (size_t)k * MODW));
; #pragma unroll
;         for (int b = 0; b < 4; ++b) { const float s = __builtin_bit_cast(float, __builtin_amdgcn_readlane(__builtin_bit_cast(int, cs[b]), k)); acc[b] += w * s; } }
	v_readlane_b32 s2, v58, 38
	v_readlane_b32 s4, v59, 38
	v_readlane_b32 s6, v60, 38
	v_readlane_b32 s8, v61, 38
	v_pk_fma_f32 v[18:19], v[70:71], s[10:11], v[18:19] op_sel_hi:[1,0,1]
	v_pk_fma_f32 v[20:21], v[72:73], s[10:11], v[20:21] op_sel_hi:[1,0,1]
	v_pk_fma_f32 v[14:15], v[70:71], s[12:13], v[14:15] op_sel_hi:[1,0,1]
	v_pk_fma_f32 v[16:17], v[72:73], s[12:13], v[16:17] op_sel_hi:[1,0,1]
	v_pk_fma_f32 v[10:11], v[70:71], s[14:15], v[10:11] op_sel_hi:[1,0,1]
	v_pk_fma_f32 v[12:13], v[72:73], s[14:15], v[12:13] op_sel_hi:[1,0,1]
	v_pk_fma_f32 v[6:7], v[70:71], s[16:17], v[6:7] op_sel_hi:[1,0,1]
	v_pk_fma_f32 v[8:9], v[72:73], s[16:17], v[8:9] op_sel_hi:[1,0,1]
	global_load_dwordx4 v[70:73], v78, s[18:19] nt
	s_add_u32 s18, s18, 0x18000
	s_addc_u32 s19, s19, 0
	s_waitcnt vmcnt(12)
	v_readlane_b32 s10, v58, 39
	v_readlane_b32 s12, v59, 39
	v_readlane_b32 s14, v60, 39
	v_readlane_b32 s16, v61, 39
	v_pk_fma_f32 v[18:19], v[74:75], s[2:3], v[18:19] op_sel_hi:[1,0,1]
	v_pk_fma_f32 v[20:21], v[76:77], s[2:3], v[20:21] op_sel_hi:[1,0,1]
	v_pk_fma_f32 v[14:15], v[74:75], s[4:5], v[14:15] op_sel_hi:[1,0,1]
	v_pk_fma_f32 v[16:17], v[76:77], s[4:5], v[16:17] op_sel_hi:[1,0,1]
	v_pk_fma_f32 v[10:11], v[74:75], s[6:7], v[10:11] op_sel_hi:[1,0,1]
	v_pk_fma_f32 v[12:13], v[76:77], s[6:7], v[12:13] op_sel_hi:[1,0,1]
	v_pk_fma_f32 v[6:7], v[74:75], s[8:9], v[6:7] op_sel_hi:[1,0,1]
	v_pk_fma_f32 v[8:9], v[76:77], s[8:9], v[8:9] op_sel_hi:[1,0,1]
	global_load_dwordx4 v[74:77], v78, s[18:19] nt
	s_add_u32 s18, s18, 0x18000
	s_addc_u32 s19, s19, 0
	s_waitcnt vmcnt(12)
	v_readlane_b32 s2, v58, 40
	v_readlane_b32 s4, v59, 40
	v_readlane_b32 s6, v60, 40
	v_readlane_b32 s8, v61, 40
	v_pk_fma_f32 v[18:19], v[2:3], s[10:11], v[18:19] op_sel_hi:[1,0,1]
	v_pk_fma_f32 v[20:21], v[4:5], s[10:11], v[20:21] op_sel_hi:[1,0,1]
	v_pk_fma_f32 v[14:15], v[2:3], s[12:13], v[14:15] op_sel_hi:[1,0,1]
	v_pk_fma_f32 v[16:17], v[4:5], s[12:13], v[16:17] op_sel_hi:[1,0,1]
	v_pk_fma_f32 v[10:11], v[2:3], s[14:15], v[10:11] op_sel_hi:[1,0,1]
	v_pk_fma_f32 v[12:13], v[4:5], s[14:15], v[12:13] op_sel_hi:[1,0,1]
	v_pk_fma_f32 v[6:7], v[2:3], s[16:17], v[6:7] op_sel_hi:[1,0,1]
	v_pk_fma_f32 v[8:9], v[4:5], s[16:17], v[8:9] op_sel_hi:[1,0,1]
	global_load_dwordx4 v[2:5], v78, s[18:19] nt
	s_add_u32 s18, s18, 0x18000
	s_addc_u32 s19, s19, 0
	s_waitcnt vmcnt(12)
	v_readlane_b32 s10, v58, 41
	v_readlane_b32 s12, v59, 41
	v_readlane_b32 s14, v60, 41
	v_readlane_b32 s16, v61, 41
	v_pk_fma_f32 v[18:19], v[22:23], s[2:3], v[18:19] op_sel_hi:[1,0,1]
	v_pk_fma_f32 v[20:21], v[24:25], s[2:3], v[20:21] op_sel_hi:[1,0,1]
	v_pk_fma_f32 v[14:15], v[22:23], s[4:5], v[14:15] op_sel_hi:[1,0,1]
	v_pk_fma_f32 v[16:17], v[24:25], s[4:5], v[16:17] op_sel_hi:[1,0,1]
	v_pk_fma_f32 v[10:11], v[22:23], s[6:7], v[10:11] op_sel_hi:[1,0,1]
	v_pk_fma_f32 v[12:13], v[24:25], s[6:7], v[12:13] op_sel_hi:[1,0,1]
	v_pk_fma_f32 v[6:7], v[22:23], s[8:9], v[6:7] op_sel_hi:[1,0,1]
	v_pk_fma_f32 v[8:9], v[24:25], s[8:9], v[8:9] op_sel_hi:[1,0,1]
	global_load_dwordx4 v[22:25], v78, s[18:19] nt
	s_add_u32 s18, s18, 0x18000
	s_addc_u32 s19, s19, 0
	s_waitcnt vmcnt(12)
	v_readlane_b32 s2, v58, 42
	v_readlane_b32 s4, v59, 42
	v_readlane_b32 s6, v60, 42
	v_readlane_b32 s8, v61, 42
	v_pk_fma_f32 v[18:19], v[26:27], s[10:11], v[18:19] op_sel_hi:[1,0,1]
	v_pk_fma_f32 v[20:21], v[28:29], s[10:11], v[20:21] op_sel_hi:[1,0,1]
	v_pk_fma_f32 v[14:15], v[26:27], s[12:13], v[14:15] op_sel_hi:[1,0,1]
	v_pk_fma_f32 v[16:17], v[28:29], s[12:13], v[16:17] op_sel_hi:[1,0,1]
	v_pk_fma_f32 v[10:11], v[26:27], s[14:15], v[10:11] op_sel_hi:[1,0,1]
	v_pk_fma_f32 v[12:13], v[28:29], s[14:15], v[12:13] op_sel_hi:[1,0,1]
	v_pk_fma_f32 v[6:7], v[26:27], s[16:17], v[6:7] op_sel_hi:[1,0,1]
	v_pk_fma_f32 v[8:9], v[28:29], s[16:17], v[8:9] op_sel_hi:[1,0,1]
	global_load_dwordx4 v[26:29], v78, s[18:19] nt
	s_add_u32 s18, s18, 0x18000
	s_addc_u32 s19, s19, 0
	s_waitcnt vmcnt(12)
	v_readlane_b32 s10, v58, 43
	v_readlane_b32 s12, v59, 43
	v_readlane_b32 s14, v60, 43
	v_readlane_b32 s16, v61, 43
	v_pk_fma_f32 v[18:19], v[30:31], s[2:3], v[18:19] op_sel_hi:[1,0,1]
	v_pk_fma_f32 v[20:21], v[32:33], s[2:3], v[20:21] op_sel_hi:[1,0,1]
	v_pk_fma_f32 v[14:15], v[30:31], s[4:5], v[14:15] op_sel_hi:[1,0,1]
	v_pk_fma_f32 v[16:17], v[32:33], s[4:5], v[16:17] op_sel_hi:[1,0,1]
	v_pk_fma_f32 v[10:11], v[30:31], s[6:7], v[10:11] op_sel_hi:[1,0,1]
	v_pk_fma_f32 v[12:13], v[32:33], s[6:7], v[12:13] op_sel_hi:[1,0,1]
	v_pk_fma_f32 v[6:7], v[30:31], s[8:9], v[6:7] op_sel_hi:[1,0,1]
	v_pk_fma_f32 v[8:9], v[32:33], s[8:9], v[8:9] op_sel_hi:[1,0,1]
	global_load_dwordx4 v[30:33], v78, s[18:19] nt
	s_add_u32 s18, s18, 0x18000
	s_addc_u32 s19, s19, 0
	s_waitcnt vmcnt(12)
	v_readlane_b32 s2, v58, 44
	v_readlane_b32 s4, v59, 44
	v_readlane_b32 s6, v60, 44
	v_readlane_b32 s8, v61, 44
	v_pk_fma_f32 v[18:19], v[34:35], s[10:11], v[18:19] op_sel_hi:[1,0,1]
	v_pk_fma_f32 v[20:21], v[36:37], s[10:11], v[20:21] op_sel_hi:[1,0,1]
	v_pk_fma_f32 v[14:15], v[34:35], s[12:13], v[14:15] op_sel_hi:[1,0,1]
	v_pk_fma_f32 v[16:17], v[36:37], s[12:13], v[16:17] op_sel_hi:[1,0,1]
	v_pk_fma_f32 v[10:11], v[34:35], s[14:15], v[10:11] op_sel_hi:[1,0,1]
	v_pk_fma_f32 v[12:13], v[36:37], s[14:15], v[12:13] op_sel_hi:[1,0,1]
	v_pk_fma_f32 v[6:7], v[34:35], s[16:17], v[6:7] op_sel_hi:[1,0,1]
	v_pk_fma_f32 v[8:9], v[36:37], s[16:17], v[8:9] op_sel_hi:[1,0,1]
	global_load_dwordx4 v[34:37], v78, s[18:19] nt
	s_add_u32 s18, s18, 0x18000
	s_addc_u32 s19, s19, 0
	s_waitcnt vmcnt(12)
; #define GAS __attribute__((address_space(1)))
; __device__ __forceinline__ void gemv_item(Frame& F, int item) {
;     ...
; #pragma unroll 16
;     for (int k = 0; k < 64; ++k) { const f32x4 w = __builtin_nontemporal_load((const GAS f32x4*)(wp + (size_t)k * MODW));
; #pragma unroll
;         for (int b = 0; b < 4; ++b) { const float s = __builtin_bit_cast(float, __builtin_amdgcn_readlane(__builtin_bit_cast(int, cs[b]), k)); acc[b] += w * s; } }
	v_readlane_b32 s10, v58, 45
	v_readlane_b32 s12, v59, 45
	v_readlane_b32 s14, v60, 45
	v_readlane_b32 s16, v61, 45
	v_pk_fma_f32 v[18:19], v[40:41], s[2:3], v[18:19] op_sel_hi:[1,0,1]
	v_pk_fma_f32 v[20:21], v[42:43], s[2:3], v[20:21] op_sel_hi:[1,0,1]
	v_pk_fma_f32 v[14:15], v[40:41], s[4:5], v[14:15] op_sel_hi:[1,0,1]
	v_pk_fma_f32 v[16:17], v[42:43], s[4:5], v[16:17] op_sel_hi:[1,0,1]
	v_pk_fma_f32 v[10:11], v[40:41], s[6:7], v[10:11] op_sel_hi:[1,0,1]
	v_pk_fma_f32 v[12:13], v[42:43], s[6:7], v[12:13] op_sel_hi:[1,0,1]
	v_pk_fma_f32 v[6:7], v[40:41], s[8:9], v[6:7] op_sel_hi:[1,0,1]
	v_pk_fma_f32 v[8:9], v[42:43], s[8:9], v[8:9] op_sel_hi:[1,0,1]
	global_load_dwordx4 v[40:43], v78, s[18:19] nt
	s_add_u32 s18, s18, 0x18000
	s_addc_u32 s19, s19, 0
	s_waitcnt vmcnt(12)
	v_readlane_b32 s2, v58, 46
	v_readlane_b32 s4, v59, 46
	v_readlane_b32 s6, v60, 46
	v_readlane_b32 s8, v61, 46
	v_pk_fma_f32 v[18:19], v[44:45], s[10:11], v[18:19] op_sel_hi:[1,0,1]
	v_pk_fma_f32 v[20:21], v[46:47], s[10:11], v[20:21] op_sel_hi:[1,0,1]
	v_pk_fma_f32 v[14:15], v[44:45], s[12:13], v[14:15] op_sel_hi:[1,0,1]
	v_pk_fma_f32 v[16:17], v[46:47], s[12:13], v[16:17] op_sel_hi:[1,0,1]
	v_pk_fma_f32 v[10:11], v[44:45], s[14:15], v[10:11] op_sel_hi:[1,0,1]
	v_pk_fma_f32 v[12:13], v[46:47], s[14:15], v[12:13] op_sel_hi:[1,0,1]
	v_pk_fma_f32 v[6:7], v[44:45], s[16:17], v[6:7] op_sel_hi:[1,0,1]
	v_pk_fma_f32 v[8:9], v[46:47], s[16:17], v[8:9] op_sel_hi:[1,0,1]
	global_load_dwordx4 v[44:47], v78, s[18:19] nt
	s_add_u32 s18, s18, 0x18000
	s_addc_u32 s19, s19, 0
	s_waitcnt vmcnt(12)
	v_readlane_b32 s10, v58, 47
	v_readlane_b32 s12, v59, 47
	v_readlane_b32 s14, v60, 47
	v_readlane_b32 s16, v61, 47
	v_pk_fma_f32 v[18:19], v[48:49], s[2:3], v[18:19] op_sel_hi:[1,0,1]
	v_pk_fma_f32 v[20:21], v[50:51], s[2:3], v[20:21] op_sel_hi:[1,0,1]
	v_pk_fma_f32 v[14:15], v[48:49], s[4:5], v[14:15] op_sel_hi:[1,0,1]
	v_pk_fma_f32 v[16:17], v[50:51], s[4:5], v[16:17] op_sel_hi:[1,0,1]
	v_pk_fma_f32 v[10:11], v[48:49], s[6:7], v[10:11] op_sel_hi:[1,0,1]
	v_pk_fma_f32 v[12:13], v[50:51], s[6:7], v[12:13] op_sel_hi:[1,0,1]
	v_pk_fma_f32 v[6:7], v[48:49], s[8:9], v[6:7] op_sel_hi:[1,0,1]
	v_pk_fma_f32 v[8:9], v[50:51], s[8:9], v[8:9] op_sel_hi:[1,0,1]
	global_load_dwordx4 v[48:51], v78, s[18:19] nt
	s_add_u32 s18, s18, 0x18000
	s_addc_u32 s19, s19, 0
	s_waitcnt vmcnt(12)
	v_readlane_b32 s2, v58, 48
	v_readlane_b32 s4, v59, 48
	v_readlane_b32 s6, v60, 48
	v_readlane_b32 s8, v61, 48
	v_pk_fma_f32 v[18:19], v[52:53], s[10:11], v[18:19] op_sel_hi:[1,0,1]
	v_pk_fma_f32 v[20:21], v[54:55], s[10:11], v[20:21] op_sel_hi:[1,0,1]
	v_pk_fma_f32 v[14:15], v[52:53], s[12:13], v[14:15] op_sel_hi:[1,0,1]
	v_pk_fma_f32 v[16:17], v[54:55], s[12:13], v[16:17] op_sel_hi:[1,0,1]
	v_pk_fma_f32 v[10:11], v[52:53], s[14:15], v[10:11] op_sel_hi:[1,0,1]
	v_pk_fma_f32 v[12:13], v[54:55], s[14:15], v[12:13] op_sel_hi:[1,0,1]
	v_pk_fma_f32 v[6:7], v[52:53], s[16:17], v[6:7] op_sel_hi:[1,0,1]
	v_pk_fma_f32 v[8:9], v[54:55], s[16:17], v[8:9] op_sel_hi:[1,0,1]
	global_load_dwordx4 v[52:55], v78, s[18:19] nt
	s_add_u32 s18, s18, 0x18000
	s_addc_u32 s19, s19, 0
	s_waitcnt vmcnt(12)
	v_readlane_b32 s10, v58, 49
	v_readlane_b32 s12, v59, 49
	v_readlane_b32 s14, v60, 49
	v_readlane_b32 s16, v61, 49
	v_pk_fma_f32 v[18:19], v[62:63], s[2:3], v[18:19] op_sel_hi:[1,0,1]
	v_pk_fma_f32 v[20:21], v[64:65], s[2:3], v[20:21] op_sel_hi:[1,0,1]
	v_pk_fma_f32 v[14:15], v[62:63], s[4:5], v[14:15] op_sel_hi:[1,0,1]
	v_pk_fma_f32 v[16:17], v[64:65], s[4:5], v[16:17] op_sel_hi:[1,0,1]
	v_pk_fma_f32 v[10:11], v[62:63], s[6:7], v[10:11] op_sel_hi:[1,0,1]
	v_pk_fma_f32 v[12:13], v[64:65], s[6:7], v[12:13] op_sel_hi:[1,0,1]
	v_pk_fma_f32 v[6:7], v[62:63], s[8:9], v[6:7] op_sel_hi:[1,0,1]
	v_pk_fma_f32 v[8:9], v[64:65], s[8:9], v[8:9] op_sel_hi:[1,0,1]
	global_load_dwordx4 v[62:65], v78, s[18:19] nt
	s_add_u32 s18, s18, 0x18000
	s_addc_u32 s19, s19, 0
	s_waitcnt vmcnt(12)
	v_readlane_b32 s2, v58, 50
	v_readlane_b32 s4, v59, 50
	v_readlane_b32 s6, v60, 50
	v_readlane_b32 s8, v61, 50
	v_pk_fma_f32 v[18:19], v[66:67], s[10:11], v[18:19] op_sel_hi:[1,0,1]
	v_pk_fma_f32 v[20:21], v[68:69], s[10:11], v[20:21] op_sel_hi:[1,0,1]
	v_pk_fma_f32 v[14:15], v[66:67], s[12:13], v[14:15] op_sel_hi:[1,0,1]
	v_pk_fma_f32 v[16:17], v[68:69], s[12:13], v[16:17] op_sel_hi:[1,0,1]
	v_pk_fma_f32 v[10:11], v[66:67], s[14:15], v[10:11] op_sel_hi:[1,0,1]
	v_pk_fma_f32 v[12:13], v[68:69], s[14:15], v[12:13] op_sel_hi:[1,0,1]
	v_pk_fma_f32 v[6:7], v[66:67], s[16:17], v[6:7] op_sel_hi:[1,0,1]
	v_pk_fma_f32 v[8:9], v[68:69], s[16:17], v[8:9] op_sel_hi:[1,0,1]
	global_load_dwordx4 v[66:69], v78, s[18:19] nt
	s_add_u32 s18, s18, 0x18000
	s_addc_u32 s19, s19, 0
	s_waitcnt vmcnt(12)
	v_readlane_b32 s10, v58, 51
	v_readlane_b32 s12, v59, 51
	v_readlane_b32 s14, v60, 51
	v_readlane_b32 s16, v61, 51
	v_pk_fma_f32 v[18:19], v[70:71], s[2:3], v[18:19] op_sel_hi:[1,0,1]
	v_pk_fma_f32 v[20:21], v[72:73], s[2:3], v[20:21] op_sel_hi:[1,0,1]
	v_pk_fma_f32 v[14:15], v[70:71], s[4:5], v[14:15] op_sel_hi:[1,0,1]
	v_pk_fma_f32 v[16:17], v[72:73], s[4:5], v[16:17] op_sel_hi:[1,0,1]
	v_pk_fma_f32 v[10:11], v[70:71], s[6:7], v[10:11] op_sel_hi:[1,0,1]
	v_pk_fma_f32 v[12:13], v[72:73], s[6:7], v[12:13] op_sel_hi:[1,0,1]
	v_pk_fma_f32 v[6:7], v[70:71], s[8:9], v[6:7] op_sel_hi:[1,0,1]
	v_pk_fma_f32 v[8:9], v[72:73], s[8:9], v[8:9] op_sel_hi:[1,0,1]
	global_load_dwordx4 v[70:73], v78, s[18:19] nt
	s_add_u32 s18, s18, 0x18000
	s_addc_u32 s19, s19, 0
	s_waitcnt vmcnt(12)
; #define GAS __attribute__((address_space(1)))
; __device__ __forceinline__ void gemv_item(Frame& F, int item) {
;     ...
; #pragma unroll 16
;     for (int k = 0; k < 64; ++k) { const f32x4 w = __builtin_nontemporal_load((const GAS f32x4*)(wp + (size_t)k * MODW));
; #pragma unroll
;         for (int b = 0; b < 4; ++b) { const float s = __builtin_bit_cast(float, __builtin_amdgcn_readlane(__builtin_bit_cast(int, cs[b]), k)); acc[b] += w * s; } }
	v_readlane_b32 s2, v58, 52
	v_readlane_b32 s4, v59, 52
	v_readlane_b32 s6, v60, 52
	v_readlane_b32 s8, v61, 52
	v_pk_fma_f32 v[18:19], v[74:75], s[10:11], v[18:19] op_sel_hi:[1,0,1]
	v_pk_fma_f32 v[20:21], v[76:77], s[10:11], v[20:21] op_sel_hi:[1,0,1]
	v_pk_fma_f32 v[14:15], v[74:75], s[12:13], v[14:15] op_sel_hi:[1,0,1]
	v_pk_fma_f32 v[16:17], v[76:77], s[12:13], v[16:17] op_sel_hi:[1,0,1]
	v_pk_fma_f32 v[10:11], v[74:75], s[14:15], v[10:11] op_sel_hi:[1,0,1]
	v_pk_fma_f32 v[12:13], v[76:77], s[14:15], v[12:13] op_sel_hi:[1,0,1]
	v_pk_fma_f32 v[6:7], v[74:75], s[16:17], v[6:7] op_sel_hi:[1,0,1]
	v_pk_fma_f32 v[8:9], v[76:77], s[16:17], v[8:9] op_sel_hi:[1,0,1]
	s_waitcnt vmcnt(11)
	v_readlane_b32 s10, v58, 53
	v_readlane_b32 s12, v59, 53
	v_readlane_b32 s14, v60, 53
	v_readlane_b32 s16, v61, 53
	v_pk_fma_f32 v[18:19], v[2:3], s[2:3], v[18:19] op_sel_hi:[1,0,1]
	v_pk_fma_f32 v[20:21], v[4:5], s[2:3], v[20:21] op_sel_hi:[1,0,1]
	v_pk_fma_f32 v[14:15], v[2:3], s[4:5], v[14:15] op_sel_hi:[1,0,1]
	v_pk_fma_f32 v[16:17], v[4:5], s[4:5], v[16:17] op_sel_hi:[1,0,1]
	v_pk_fma_f32 v[10:11], v[2:3], s[6:7], v[10:11] op_sel_hi:[1,0,1]
	v_pk_fma_f32 v[12:13], v[4:5], s[6:7], v[12:13] op_sel_hi:[1,0,1]
	v_pk_fma_f32 v[6:7], v[2:3], s[8:9], v[6:7] op_sel_hi:[1,0,1]
	v_pk_fma_f32 v[8:9], v[4:5], s[8:9], v[8:9] op_sel_hi:[1,0,1]
	s_waitcnt vmcnt(10)
	v_readlane_b32 s2, v58, 54
	v_readlane_b32 s4, v59, 54
	v_readlane_b32 s6, v60, 54
	v_readlane_b32 s8, v61, 54
	v_pk_fma_f32 v[18:19], v[22:23], s[10:11], v[18:19] op_sel_hi:[1,0,1]
	v_pk_fma_f32 v[20:21], v[24:25], s[10:11], v[20:21] op_sel_hi:[1,0,1]
	v_pk_fma_f32 v[14:15], v[22:23], s[12:13], v[14:15] op_sel_hi:[1,0,1]
	v_pk_fma_f32 v[16:17], v[24:25], s[12:13], v[16:17] op_sel_hi:[1,0,1]
	v_pk_fma_f32 v[10:11], v[22:23], s[14:15], v[10:11] op_sel_hi:[1,0,1]
	v_pk_fma_f32 v[12:13], v[24:25], s[14:15], v[12:13] op_sel_hi:[1,0,1]
	v_pk_fma_f32 v[6:7], v[22:23], s[16:17], v[6:7] op_sel_hi:[1,0,1]
	v_pk_fma_f32 v[8:9], v[24:25], s[16:17], v[8:9] op_sel_hi:[1,0,1]
	s_waitcnt vmcnt(9)
	v_readlane_b32 s10, v58, 55
	v_readlane_b32 s12, v59, 55
	v_readlane_b32 s14, v60, 55
	v_readlane_b32 s16, v61, 55
	v_pk_fma_f32 v[18:19], v[26:27], s[2:3], v[18:19] op_sel_hi:[1,0,1]
	v_pk_fma_f32 v[20:21], v[28:29], s[2:3], v[20:21] op_sel_hi:[1,0,1]
	v_pk_fma_f32 v[14:15], v[26:27], s[4:5], v[14:15] op_sel_hi:[1,0,1]
	v_pk_fma_f32 v[16:17], v[28:29], s[4:5], v[16:17] op_sel_hi:[1,0,1]
	v_pk_fma_f32 v[10:11], v[26:27], s[6:7], v[10:11] op_sel_hi:[1,0,1]
	v_pk_fma_f32 v[12:13], v[28:29], s[6:7], v[12:13] op_sel_hi:[1,0,1]
	v_pk_fma_f32 v[6:7], v[26:27], s[8:9], v[6:7] op_sel_hi:[1,0,1]
	v_pk_fma_f32 v[8:9], v[28:29], s[8:9], v[8:9] op_sel_hi:[1,0,1]
	s_waitcnt vmcnt(8)
	v_readlane_b32 s2, v58, 56
	v_readlane_b32 s4, v59, 56
	v_readlane_b32 s6, v60, 56
	v_readlane_b32 s8, v61, 56
	v_pk_fma_f32 v[18:19], v[30:31], s[10:11], v[18:19] op_sel_hi:[1,0,1]
	v_pk_fma_f32 v[20:21], v[32:33], s[10:11], v[20:21] op_sel_hi:[1,0,1]
	v_pk_fma_f32 v[14:15], v[30:31], s[12:13], v[14:15] op_sel_hi:[1,0,1]
	v_pk_fma_f32 v[16:17], v[32:33], s[12:13], v[16:17] op_sel_hi:[1,0,1]
	v_pk_fma_f32 v[10:11], v[30:31], s[14:15], v[10:11] op_sel_hi:[1,0,1]
	v_pk_fma_f32 v[12:13], v[32:33], s[14:15], v[12:13] op_sel_hi:[1,0,1]
	v_pk_fma_f32 v[6:7], v[30:31], s[16:17], v[6:7] op_sel_hi:[1,0,1]
	v_pk_fma_f32 v[8:9], v[32:33], s[16:17], v[8:9] op_sel_hi:[1,0,1]
	s_waitcnt vmcnt(7)
	v_readlane_b32 s10, v58, 57
	v_readlane_b32 s12, v59, 57
	v_readlane_b32 s14, v60, 57
	v_readlane_b32 s16, v61, 57
	v_pk_fma_f32 v[18:19], v[34:35], s[2:3], v[18:19] op_sel_hi:[1,0,1]
	v_pk_fma_f32 v[20:21], v[36:37], s[2:3], v[20:21] op_sel_hi:[1,0,1]
	v_pk_fma_f32 v[14:15], v[34:35], s[4:5], v[14:15] op_sel_hi:[1,0,1]
	v_pk_fma_f32 v[16:17], v[36:37], s[4:5], v[16:17] op_sel_hi:[1,0,1]
	v_pk_fma_f32 v[10:11], v[34:35], s[6:7], v[10:11] op_sel_hi:[1,0,1]
	v_pk_fma_f32 v[12:13], v[36:37], s[6:7], v[12:13] op_sel_hi:[1,0,1]
	v_pk_fma_f32 v[6:7], v[34:35], s[8:9], v[6:7] op_sel_hi:[1,0,1]
	v_pk_fma_f32 v[8:9], v[36:37], s[8:9], v[8:9] op_sel_hi:[1,0,1]
	s_waitcnt vmcnt(6)
	v_readlane_b32 s2, v58, 58
	v_readlane_b32 s4, v59, 58
	v_readlane_b32 s6, v60, 58
	v_readlane_b32 s8, v61, 58
	v_pk_fma_f32 v[18:19], v[40:41], s[10:11], v[18:19] op_sel_hi:[1,0,1]
	v_pk_fma_f32 v[20:21], v[42:43], s[10:11], v[20:21] op_sel_hi:[1,0,1]
	v_pk_fma_f32 v[14:15], v[40:41], s[12:13], v[14:15] op_sel_hi:[1,0,1]
	v_pk_fma_f32 v[16:17], v[42:43], s[12:13], v[16:17] op_sel_hi:[1,0,1]
	v_pk_fma_f32 v[10:11], v[40:41], s[14:15], v[10:11] op_sel_hi:[1,0,1]
	v_pk_fma_f32 v[12:13], v[42:43], s[14:15], v[12:13] op_sel_hi:[1,0,1]
	v_pk_fma_f32 v[6:7], v[40:41], s[16:17], v[6:7] op_sel_hi:[1,0,1]
	v_pk_fma_f32 v[8:9], v[42:43], s[16:17], v[8:9] op_sel_hi:[1,0,1]
	s_waitcnt vmcnt(5)
; #define GAS __attribute__((address_space(1)))
; __device__ __forceinline__ void gemv_item(Frame& F, int item) {
;     ...
; #pragma unroll 16
;     for (int k = 0; k < 64; ++k) { const f32x4 w = __builtin_nontemporal_load((const GAS f32x4*)(wp + (size_t)k * MODW));
; #pragma unroll
;         for (int b = 0; b < 4; ++b) { const float s = __builtin_bit_cast(float, __builtin_amdgcn_readlane(__builtin_bit_cast(int, cs[b]), k)); acc[b] += w * s; } }
; #pragma unroll
;     for (int b = 0; b < 4; ++b) *(GAS f32x4*)(F.PART + (size_t)(ks * 4 + b) * MODW + n0) = acc[b];
; __device__ __forceinline__ void p0_prologue(Frame& F, bool with_gemv = true) {
;     ...
;     if (with_gemv) for (int it = F.gw; it < I_GV; it += F.NGW) gemv_item(F, it);
	v_readlane_b32 s10, v58, 59
	v_readlane_b32 s12, v59, 59
	v_readlane_b32 s14, v60, 59
	v_readlane_b32 s16, v61, 59
	v_pk_fma_f32 v[18:19], v[44:45], s[2:3], v[18:19] op_sel_hi:[1,0,1]
	v_pk_fma_f32 v[20:21], v[46:47], s[2:3], v[20:21] op_sel_hi:[1,0,1]
	v_pk_fma_f32 v[14:15], v[44:45], s[4:5], v[14:15] op_sel_hi:[1,0,1]
	v_pk_fma_f32 v[16:17], v[46:47], s[4:5], v[16:17] op_sel_hi:[1,0,1]
	v_pk_fma_f32 v[10:11], v[44:45], s[6:7], v[10:11] op_sel_hi:[1,0,1]
	v_pk_fma_f32 v[12:13], v[46:47], s[6:7], v[12:13] op_sel_hi:[1,0,1]
	v_pk_fma_f32 v[6:7], v[44:45], s[8:9], v[6:7] op_sel_hi:[1,0,1]
	v_pk_fma_f32 v[8:9], v[46:47], s[8:9], v[8:9] op_sel_hi:[1,0,1]
	s_waitcnt vmcnt(4)
	v_readlane_b32 s2, v58, 60
	v_readlane_b32 s4, v59, 60
	v_readlane_b32 s6, v60, 60
	v_readlane_b32 s8, v61, 60
	v_pk_fma_f32 v[18:19], v[48:49], s[10:11], v[18:19] op_sel_hi:[1,0,1]
	v_pk_fma_f32 v[20:21], v[50:51], s[10:11], v[20:21] op_sel_hi:[1,0,1]
	v_pk_fma_f32 v[14:15], v[48:49], s[12:13], v[14:15] op_sel_hi:[1,0,1]
	v_pk_fma_f32 v[16:17], v[50:51], s[12:13], v[16:17] op_sel_hi:[1,0,1]
	v_pk_fma_f32 v[10:11], v[48:49], s[14:15], v[10:11] op_sel_hi:[1,0,1]
	v_pk_fma_f32 v[12:13], v[50:51], s[14:15], v[12:13] op_sel_hi:[1,0,1]
	v_pk_fma_f32 v[6:7], v[48:49], s[16:17], v[6:7] op_sel_hi:[1,0,1]
	v_pk_fma_f32 v[8:9], v[50:51], s[16:17], v[8:9] op_sel_hi:[1,0,1]
	s_waitcnt vmcnt(3)
	v_readlane_b32 s10, v58, 61
	v_readlane_b32 s12, v59, 61
	v_readlane_b32 s14, v60, 61
	v_readlane_b32 s16, v61, 61
	v_pk_fma_f32 v[18:19], v[52:53], s[2:3], v[18:19] op_sel_hi:[1,0,1]
	v_pk_fma_f32 v[20:21], v[54:55], s[2:3], v[20:21] op_sel_hi:[1,0,1]
	v_pk_fma_f32 v[14:15], v[52:53], s[4:5], v[14:15] op_sel_hi:[1,0,1]
	v_pk_fma_f32 v[16:17], v[54:55], s[4:5], v[16:17] op_sel_hi:[1,0,1]
	v_pk_fma_f32 v[10:11], v[52:53], s[6:7], v[10:11] op_sel_hi:[1,0,1]
	v_pk_fma_f32 v[12:13], v[54:55], s[6:7], v[12:13] op_sel_hi:[1,0,1]
	v_pk_fma_f32 v[6:7], v[52:53], s[8:9], v[6:7] op_sel_hi:[1,0,1]
	v_pk_fma_f32 v[8:9], v[54:55], s[8:9], v[8:9] op_sel_hi:[1,0,1]
	s_waitcnt vmcnt(2)
	v_readlane_b32 s2, v58, 62
	v_readlane_b32 s4, v59, 62
	v_readlane_b32 s6, v60, 62
	v_readlane_b32 s8, v61, 62
	v_pk_fma_f32 v[18:19], v[62:63], s[10:11], v[18:19] op_sel_hi:[1,0,1]
	v_pk_fma_f32 v[20:21], v[64:65], s[10:11], v[20:21] op_sel_hi:[1,0,1]
	v_pk_fma_f32 v[14:15], v[62:63], s[12:13], v[14:15] op_sel_hi:[1,0,1]
	v_pk_fma_f32 v[16:17], v[64:65], s[12:13], v[16:17] op_sel_hi:[1,0,1]
	v_pk_fma_f32 v[10:11], v[62:63], s[14:15], v[10:11] op_sel_hi:[1,0,1]
	v_pk_fma_f32 v[12:13], v[64:65], s[14:15], v[12:13] op_sel_hi:[1,0,1]
	v_pk_fma_f32 v[6:7], v[62:63], s[16:17], v[6:7] op_sel_hi:[1,0,1]
	v_pk_fma_f32 v[8:9], v[64:65], s[16:17], v[8:9] op_sel_hi:[1,0,1]
	s_waitcnt vmcnt(1)
	v_readlane_b32 s10, v58, 63
	v_readlane_b32 s12, v59, 63
	v_readlane_b32 s14, v60, 63
	v_readlane_b32 s16, v61, 63
	v_pk_fma_f32 v[18:19], v[66:67], s[2:3], v[18:19] op_sel_hi:[1,0,1]
	v_pk_fma_f32 v[20:21], v[68:69], s[2:3], v[20:21] op_sel_hi:[1,0,1]
	v_pk_fma_f32 v[14:15], v[66:67], s[4:5], v[14:15] op_sel_hi:[1,0,1]
	v_pk_fma_f32 v[16:17], v[68:69], s[4:5], v[16:17] op_sel_hi:[1,0,1]
	v_pk_fma_f32 v[10:11], v[66:67], s[6:7], v[10:11] op_sel_hi:[1,0,1]
	v_pk_fma_f32 v[12:13], v[68:69], s[6:7], v[12:13] op_sel_hi:[1,0,1]
	v_pk_fma_f32 v[6:7], v[66:67], s[8:9], v[6:7] op_sel_hi:[1,0,1]
	v_pk_fma_f32 v[8:9], v[68:69], s[8:9], v[8:9] op_sel_hi:[1,0,1]
	s_waitcnt vmcnt(0)
	v_pk_fma_f32 v[18:19], v[70:71], s[10:11], v[18:19] op_sel_hi:[1,0,1]
	v_pk_fma_f32 v[20:21], v[72:73], s[10:11], v[20:21] op_sel_hi:[1,0,1]
	v_pk_fma_f32 v[14:15], v[70:71], s[12:13], v[14:15] op_sel_hi:[1,0,1]
	v_pk_fma_f32 v[16:17], v[72:73], s[12:13], v[16:17] op_sel_hi:[1,0,1]
	v_pk_fma_f32 v[10:11], v[70:71], s[14:15], v[10:11] op_sel_hi:[1,0,1]
	v_pk_fma_f32 v[12:13], v[72:73], s[14:15], v[12:13] op_sel_hi:[1,0,1]
	v_pk_fma_f32 v[6:7], v[70:71], s[16:17], v[6:7] op_sel_hi:[1,0,1]
	v_pk_fma_f32 v[8:9], v[72:73], s[16:17], v[8:9] op_sel_hi:[1,0,1]
	s_mov_b32 s43, 64
	s_lshl_b32 s2, s41, 2
	s_mul_i32 s41, s41, 0x60000
	s_mul_hi_i32 s1, s2, 0x18000
	s_add_u32 s0, s31, s41
	s_addc_u32 s1, s33, s1
	v_lshlrev_b64 v[2:3], 2, v[38:39]
	v_lshl_add_u64 v[4:5], s[0:1], 0, v[2:3]
	s_or_b32 s0, s2, 1
	s_mul_hi_i32 s1, s0, 0x18000
	s_mul_i32 s0, s0, 0x18000
	s_add_u32 s0, s31, s0
	s_addc_u32 s1, s33, s1
	global_store_dwordx4 v[4:5], v[18:21], off
	v_lshl_add_u64 v[4:5], s[0:1], 0, v[2:3]
	s_or_b32 s0, s2, 2
	s_mul_hi_i32 s1, s0, 0x18000
	s_mul_i32 s0, s0, 0x18000
	s_add_u32 s0, s31, s0
	s_addc_u32 s1, s33, s1
	global_store_dwordx4 v[4:5], v[14:17], off
	v_lshl_add_u64 v[4:5], s[0:1], 0, v[2:3]
	s_or_b32 s0, s2, 3
	s_mul_hi_i32 s1, s0, 0x18000
	s_mul_i32 s0, s0, 0x18000
	s_add_u32 s0, s31, s0
	s_addc_u32 s1, s33, s1
	s_add_i32 s39, s39, s86
	v_lshl_add_u64 v[2:3], s[0:1], 0, v[2:3]
	s_cmpk_lt_i32 s39, 0x1800
	global_store_dwordx4 v[4:5], v[10:13], off
	global_store_dwordx4 v[2:3], v[6:9], off
	s_cbranch_scc1 .LBB0_10

; #define GAS __attribute__((address_space(1)))
; __device__ __forceinline__ void qk_load(Frame& F, int row, QkRow& R) {
;     const bf16* prow = F.PROJ + (size_t)row * PNP; const int lane = F.lane;
; #pragma unroll
;     for (int i = 0; i < 4; ++i) { R.q[i] = ((const GAS v4u*)(prow + PQ + 32 * lane))[i]; R.g[i] = ((const GAS v4u*)(prow + PGV + 32 * lane))[i]; }
;     R.k = *(const GAS v4u*)(prow + PK + 8 * lane);
; }
; __device__ __forceinline__ void qknorm_rows(Frame& F) {
;     QkRow A, B; int row = F.gw; bool hasA = row < M;
;     if (hasA) qk_load(F, row, A);
.LBB0_1214:
	v_readlane_b32 s0, v249, 38
	v_readlane_b32 s26, v248, 42
	v_readlane_b32 s28, v248, 40
	v_readlane_b32 s30, v248, 38
	v_readlane_b32 s56, v248, 36
	s_cmpk_gt_i32 s0, 0x1fff
	v_readlane_b32 s27, v248, 43
	v_readlane_b32 s29, v248, 41
	v_readlane_b32 s31, v248, 39
	v_readlane_b32 s57, v248, 37
	v_readlane_b32 s1, v249, 39
	s_cbranch_scc1 .LBB0_1241
	v_readlane_b32 s20, v249, 27
	v_readlane_b32 s21, v249, 28
	v_readlane_b32 s22, v249, 29
	v_readlane_b32 s23, v249, 30
	v_lshlrev_b32_e32 v230, 7, v180
	v_and_b32_e32 v230, 0x180, v230
	v_lshlrev_b32_e32 v231, 5, v180
	v_and_b32_e32 v231, 0x1e0, v231
	s_nop 4
	global_load_dwordx4 v[190:193], v230, s[20:21]
	global_load_dwordx4 v[194:197], v230, s[20:21] offset:16
	global_load_dwordx4 v[198:201], v230, s[20:21] offset:32
	global_load_dwordx4 v[202:205], v230, s[20:21] offset:48
	global_load_dwordx4 v[206:209], v230, s[20:21] offset:64
	global_load_dwordx4 v[210:213], v230, s[20:21] offset:80
	global_load_dwordx4 v[214:217], v230, s[20:21] offset:96
	global_load_dwordx4 v[218:221], v230, s[20:21] offset:112
	global_load_dwordx4 v[222:225], v231, s[22:23]
	global_load_dwordx4 v[226:229], v231, s[22:23] offset:16
	v_readlane_b32 s6, v249, 38
	s_mul_i32 s0, s6, 0x8a00
	v_readlane_b32 s2, v248, 12
	s_mul_hi_i32 s1, s6, 0x8a00
	v_readlane_b32 s3, v248, 13
	s_add_u32 s0, s2, s0
	s_addc_u32 s1, s3, s1
	v_mov_b32_e32 v91, 0
	v_lshl_add_u64 v[14:15], s[0:1], 0, v[90:91]
	s_mov_b64 s[4:5], 0x3800
	s_movk_i32 s15, 0x3000
	v_lshl_add_u64 v[30:31], v[14:15], 0, s[4:5]
	global_load_dwordx4 v[2:5], v90, s[0:1] offset:48
	global_load_dwordx4 v[6:9], v90, s[0:1] offset:32
	global_load_dwordx4 v[10:13], v90, s[0:1] offset:16
	global_load_dwordx4 v[26:29], v90, s[0:1]
	v_add_co_u32_e32 v14, vcc, s15, v14
	v_lshlrev_b32_e32 v90, 4, v180
	s_nop 0
	v_addc_co_u32_e32 v15, vcc, 0, v15, vcc
	v_lshl_add_u64 v[34:35], s[0:1], 0, v[90:91]
	s_movk_i32 s16, 0x1000
	global_load_dwordx4 v[14:17], v[14:15], off offset:2048
	s_nop 0
	global_load_dwordx4 v[18:21], v[30:31], off offset:48
	global_load_dwordx4 v[22:25], v[30:31], off offset:32
	s_nop 0
	global_load_dwordx4 v[30:33], v[30:31], off offset:16
	v_add_co_u32_e32 v34, vcc, s16, v34
	v_readlane_b32 s56, v249, 15
	s_nop 0
	v_addc_co_u32_e32 v35, vcc, 0, v35, vcc
	global_load_dwordx4 v[46:49], v[34:35], off
	v_lshlrev_b32_e32 v1, 7, v180
	v_readlane_b32 s68, v249, 27
	v_readlane_b32 s69, v249, 28
	v_lshlrev_b32_e32 v34, 5, v180
	v_and_b32_e32 v90, 0x180, v1
	v_readlane_b32 s70, v249, 29
	v_readlane_b32 s71, v249, 30
	s_mov_b64 s[20:21], s[68:69]
	s_mov_b64 s[22:23], s[70:71]
	v_lshl_add_u64 v[74:75], s[20:21], 0, v[90:91]
	v_and_b32_e32 v90, 0x1e0, v34
	v_lshl_add_u64 v[76:77], s[22:23], 0, v[90:91]
	v_cmp_eq_u32_e64 s[2:3], 0, v180
	s_lshl_b32 s14, s89, 4
	v_mov_b32_e32 v1, 0x358637bd
	s_mov_b32 s17, 0xf800000
	s_waitcnt vmcnt(9)
	v_mov_b32_e32 v80, 0x260
	s_mov_b32 s18, 0x3e0293ee
	v_lshlrev_b32_e32 v78, 1, v34
	v_lshlrev_b32_e32 v90, 1, v184
	s_mov_b32 s8, s6
	v_readlane_b32 s7, v249, 39
	v_readlane_b32 s57, v249, 16
	v_readlane_b32 s58, v249, 17
	v_readlane_b32 s59, v249, 18
	v_readlane_b32 s60, v249, 19
	v_readlane_b32 s61, v249, 20
	v_readlane_b32 s62, v249, 21
	v_readlane_b32 s63, v249, 22
	v_readlane_b32 s64, v249, 23
	v_readlane_b32 s65, v249, 24
	v_readlane_b32 s66, v249, 25
	v_readlane_b32 s67, v249, 26
	s_branch .LBB0_1218

; #define GAS __attribute__((address_space(1)))
; __device__ __forceinline__ unsigned pk2(float lo, float hi) { return pg8::cvt_pk_bf16(lo, hi); }
; __device__ __forceinline__ float sum4(float v) { v += dpp_f<0xB1>(v); v += dpp_f<0x4E>(v); return v; }
; __device__ __forceinline__ void qk_finish(Frame& F, int row, const QkRow& R) {
;     bf16* prow = F.PROJ + (size_t)row * PNP; const int lane = F.lane;
;     {
;         float ss = 0.f;
; #pragma unroll
;         for (int i = 0; i < 4; ++i)
; #pragma unroll
;             for (int j = 0; j < 4; ++j) { const float a = bflo(R.q[i][j]), c = bfhi(R.q[i][j]); ss += a * a + c * c; }
;         ss = sum4(ss);
;         const float r = QSCALE / sqrtf(ss * (1.f / HD) + EPS); const float* g = F.qng + 32 * (lane & 3);
; #pragma unroll
;         for (int i = 0; i < 4; ++i) { v4u o;
; #pragma unroll
;             for (int j = 0; j < 4; ++j) o[j] = pk2(bflo(R.q[i][j]) * r * g[8 * i + 2 * j], bfhi(R.q[i][j]) * r * g[8 * i + 2 * j + 1]);
;             ((GAS v4u*)(prow + PQ + 32 * lane))[i] = o; }
.LBB0_1220:
	s_waitcnt vmcnt(9)
	v_and_b32_e32 v81, 0xffff0000, v26
	v_and_b32_e32 v93, 0xffff0000, v27
	v_lshlrev_b32_e32 v79, 16, v26
	v_mul_f32_e32 v82, v81, v81
	v_lshlrev_b32_e32 v92, 16, v27
	v_mul_f32_e32 v83, v93, v93
	v_fmac_f32_e32 v82, v79, v79
	v_fmac_f32_e32 v83, v92, v92
	v_and_b32_e32 v95, 0xffff0000, v28
	v_add_f32_e32 v82, v82, v83
	v_lshlrev_b32_e32 v94, 16, v28
	v_mul_f32_e32 v83, v95, v95
	v_fmac_f32_e32 v83, v94, v94
	v_and_b32_e32 v97, 0xffff0000, v29
	v_add_f32_e32 v82, v83, v82
	v_lshlrev_b32_e32 v96, 16, v29
	v_mul_f32_e32 v83, v97, v97
	v_fmac_f32_e32 v83, v96, v96
	v_and_b32_e32 v99, 0xffff0000, v10
	v_add_f32_e32 v82, v83, v82
	v_lshlrev_b32_e32 v98, 16, v10
	v_mul_f32_e32 v83, v99, v99
	v_fmac_f32_e32 v83, v98, v98
	v_and_b32_e32 v101, 0xffff0000, v11
	v_add_f32_e32 v82, v83, v82
	v_lshlrev_b32_e32 v100, 16, v11
	v_mul_f32_e32 v83, v101, v101
	v_fmac_f32_e32 v83, v100, v100
	v_and_b32_e32 v103, 0xffff0000, v12
	v_add_f32_e32 v82, v83, v82
	v_lshlrev_b32_e32 v102, 16, v12
	v_mul_f32_e32 v83, v103, v103
	v_fmac_f32_e32 v83, v102, v102
	v_add_f32_e32 v84, v83, v82
	v_and_b32_e32 v105, 0xffff0000, v13
	v_lshlrev_b32_e32 v104, 16, v13
	v_mul_f32_e32 v85, v105, v105
	v_fmac_f32_e32 v85, v104, v104
	v_and_b32_e32 v107, 0xffff0000, v6
	v_add_f32_e32 v84, v85, v84
	v_lshlrev_b32_e32 v106, 16, v6
	v_mul_f32_e32 v85, v107, v107
	v_fmac_f32_e32 v85, v106, v106
	v_and_b32_e32 v109, 0xffff0000, v7
	v_add_f32_e32 v84, v85, v84
	v_lshlrev_b32_e32 v108, 16, v7
	v_mul_f32_e32 v85, v109, v109
	v_fmac_f32_e32 v85, v108, v108
	v_and_b32_e32 v111, 0xffff0000, v8
	v_add_f32_e32 v84, v85, v84
	v_lshlrev_b32_e32 v110, 16, v8
	v_mul_f32_e32 v85, v111, v111
	v_fmac_f32_e32 v85, v110, v110
	v_and_b32_e32 v113, 0xffff0000, v9
	v_add_f32_e32 v84, v85, v84
	v_lshlrev_b32_e32 v112, 16, v9
	v_mul_f32_e32 v85, v113, v113
	v_fmac_f32_e32 v85, v112, v112
	v_and_b32_e32 v115, 0xffff0000, v2
	v_add_f32_e32 v84, v85, v84
	v_lshlrev_b32_e32 v114, 16, v2
	v_mul_f32_e32 v85, v115, v115
	v_fmac_f32_e32 v85, v114, v114
	v_and_b32_e32 v117, 0xffff0000, v3
	v_add_f32_e32 v84, v85, v84
	v_lshlrev_b32_e32 v116, 16, v3
	v_mul_f32_e32 v85, v117, v117
	v_fmac_f32_e32 v85, v116, v116
	v_and_b32_e32 v89, 0xffff0000, v5
	v_and_b32_e32 v88, 0xffff0000, v4
	v_add_f32_e32 v118, v85, v84
	v_lshlrev_b32_e32 v87, 16, v5
	v_lshlrev_b32_e32 v86, 16, v4
	v_pk_mul_f32 v[84:85], v[88:89], v[88:89]
	v_readlane_b32 s12, v248, 12
	v_pk_fma_f32 v[84:85], v[86:87], v[86:87], v[84:85]
	v_readlane_b32 s13, v248, 13
	v_add_f32_e32 v84, v84, v118
	v_add_f32_e32 v84, v85, v84
	s_nop 1
	v_add_f32_dpp v84, v84, v84 quad_perm:[1,0,3,2] row_mask:0xf bank_mask:0xf bound_ctrl:1
	s_nop 1
	v_add_f32_dpp v84, v84, v84 quad_perm:[2,3,0,1] row_mask:0xf bank_mask:0xf bound_ctrl:1
	v_fmamk_f32 v84, v84, 0x3c000000, v1
	v_mul_f32_e32 v85, 0x4f800000, v84
	v_cmp_gt_f32_e32 vcc, s17, v84
	s_nop 1
	v_cndmask_b32_e32 v84, v84, v85, vcc
	v_sqrt_f32_e32 v85, v84
	s_nop 0
	v_add_u32_e32 v118, -1, v85
	v_fma_f32 v119, -v118, v85, v84
	v_cmp_ge_f32_e64 s[0:1], 0, v119
	v_add_u32_e32 v119, 1, v85
	s_nop 0
	v_cndmask_b32_e64 v118, v85, v118, s[0:1]
	v_fma_f32 v85, -v119, v85, v84
	v_cmp_lt_f32_e64 s[0:1], 0, v85
	s_nop 1
	v_cndmask_b32_e64 v85, v118, v119, s[0:1]
	v_mul_f32_e32 v118, 0x37800000, v85
	v_cndmask_b32_e32 v85, v85, v118, vcc
	v_cmp_class_f32_e32 vcc, v84, v80
	s_nop 1
	v_cndmask_b32_e32 v84, v85, v84, vcc
	v_div_scale_f32 v85, s[0:1], v84, v84, s18
	v_rcp_f32_e32 v118, v85
	s_mul_i32 s1, s8, 0x8a00
	s_mul_hi_i32 s0, s8, 0x8a00
	s_add_u32 s12, s12, s1
	v_fma_f32 v119, -v85, v118, 1.0
	v_fmac_f32_e32 v118, v119, v118
	v_div_scale_f32 v119, vcc, s18, v84, s18
	v_mul_f32_e32 v120, v119, v118
	v_fma_f32 v121, -v85, v120, v119
	v_fmac_f32_e32 v120, v121, v118
	v_fma_f32 v85, -v85, v120, v119
	v_div_fmas_f32 v85, v85, v118, v120
	v_div_fixup_f32 v118, v85, v84, s18
	v_mul_f32_e32 v79, v118, v79
	v_mul_f32_e32 v81, v118, v81
	v_mul_f32_e32 v79, v190, v79
	v_mul_f32_e32 v81, v191, v81
	v_cvt_pk_bf16_f32 v82, v79, v81
	v_mul_f32_e32 v79, v118, v92
	v_mul_f32_e32 v81, v118, v93
	s_addc_u32 s13, s13, s0
	v_and_b32_e32 v119, 0xffff0000, v20
	v_and_b32_e32 v121, 0xffff0000, v21
	v_mul_f32_e32 v119, v119, v119
	v_lshlrev_b32_e32 v120, 16, v21
	v_mul_f32_e32 v121, v121, v121
	v_fmac_f32_e32 v121, v120, v120
	v_mul_f32_e32 v79, v192, v79
	v_mul_f32_e32 v81, v193, v81
	v_cvt_pk_bf16_f32 v83, v79, v81
	v_mul_f32_e32 v79, v118, v94
	v_mul_f32_e32 v81, v118, v95
	v_mul_f32_e32 v79, v79, v194
	v_mul_f32_e32 v81, v81, v195
	v_cvt_pk_bf16_f32 v84, v79, v81
	v_mul_f32_e32 v79, v118, v96
	v_mul_f32_e32 v81, v118, v97
	v_mul_f32_e32 v79, v79, v196
	v_mul_f32_e32 v81, v81, v197
	v_cvt_pk_bf16_f32 v85, v79, v81
	global_store_dwordx4 v78, v[82:85], s[12:13]
	v_mul_f32_e32 v79, v118, v98
	v_mul_f32_e32 v81, v118, v99
	v_and_b32_e32 v98, 0xffff0000, v16
	v_mul_f32_e32 v98, v98, v98
	v_lshlrev_b32_e32 v99, 16, v17
	v_mul_f32_e32 v79, v79, v198
	v_mul_f32_e32 v81, v81, v199
	v_cvt_pk_bf16_f32 v82, v79, v81
	v_mul_f32_e32 v79, v118, v100
	v_mul_f32_e32 v81, v118, v101
	v_and_b32_e32 v100, 0xffff0000, v17
	v_mul_f32_e32 v100, v100, v100
	v_lshlrev_b32_e32 v101, 16, v30
	v_fmac_f32_e32 v100, v99, v99
	v_mul_f32_e32 v79, v79, v200
	v_mul_f32_e32 v81, v81, v201
	v_cvt_pk_bf16_f32 v83, v79, v81
	v_mul_f32_e32 v79, v118, v102
	v_mul_f32_e32 v81, v118, v103
	v_and_b32_e32 v102, 0xffff0000, v30
	v_mul_f32_e32 v102, v102, v102
	v_lshlrev_b32_e32 v103, 16, v31
	v_fmac_f32_e32 v102, v101, v101
	v_mul_f32_e32 v79, v79, v202
	v_mul_f32_e32 v81, v81, v203
	v_cvt_pk_bf16_f32 v84, v79, v81
	v_mul_f32_e32 v79, v118, v104
	v_mul_f32_e32 v81, v118, v105
; #define GAS __attribute__((address_space(1)))
; __device__ __forceinline__ unsigned pk2(float lo, float hi) { return pg8::cvt_pk_bf16(lo, hi); }
; __device__ __forceinline__ float sum16(float v) { v = sum4(v); v += dpp_f<0x141>(v); v += dpp_f<0x140>(v); return v; }
; __device__ __forceinline__ void qk_finish(Frame& F, int row, const QkRow& R) {
;     ...
;         for (int i = 0; i < 4; ++i) { v4u o;
; #pragma unroll
;             for (int j = 0; j < 4; ++j) o[j] = pk2(bflo(R.q[i][j]) * r * g[8 * i + 2 * j], bfhi(R.q[i][j]) * r * g[8 * i + 2 * j + 1]);
;             ((GAS v4u*)(prow + PQ + 32 * lane))[i] = o; }
;     }
;     {
;         float ss = 0.f;
; #pragma unroll
;         for (int j = 0; j < 4; ++j) { const float a = bflo(R.k[j]), c = bfhi(R.k[j]); ss += a * a + c * c; }
;         ss = sum16(ss);
;         const float r = 1.0f / sqrtf(ss * (1.f / HD) + EPS); const float* g = F.kng + 8 * (lane & 15); v4u o;
; #pragma unroll
;         for (int j = 0; j < 4; ++j) o[j] = pk2(bflo(R.k[j]) * r * g[2 * j], bfhi(R.k[j]) * r * g[2 * j + 1]);
;         *(GAS v4u*)(prow + PK + 8 * lane) = o;
;     }
;     {
;         float ss = 0.f;
; #pragma unroll
;         for (int i = 0; i < 4; ++i)
; #pragma unroll
;             for (int j = 0; j < 4; ++j) { const float a = bflo(R.g[i][j]), c = bfhi(R.g[i][j]); ss += a * a + c * c; }
;         ss = wave_sum(ss);
	v_and_b32_e32 v104, 0xffff0000, v31
	v_mul_f32_e32 v104, v104, v104
	v_and_b32_e32 v105, 0xffff0000, v33
	v_fmac_f32_e32 v104, v103, v103
	v_mul_f32_e32 v105, v105, v105
	v_mul_f32_e32 v79, v79, v204
	v_mul_f32_e32 v81, v81, v205
	v_cvt_pk_bf16_f32 v85, v79, v81
	global_store_dwordx4 v78, v[82:85], s[12:13] offset:16
	v_mul_f32_e32 v79, v118, v106
	v_mul_f32_e32 v81, v118, v107
	v_and_b32_e32 v107, 0xffff0000, v22
	v_lshlrev_b32_e32 v106, 16, v22
	v_mul_f32_e32 v107, v107, v107
	v_fmac_f32_e32 v107, v106, v106
	v_mul_f32_e32 v79, v79, v206
	v_mul_f32_e32 v81, v81, v207
	v_cvt_pk_bf16_f32 v82, v79, v81
	v_mul_f32_e32 v79, v118, v108
	v_mul_f32_e32 v81, v118, v109
	v_and_b32_e32 v109, 0xffff0000, v23
	v_lshlrev_b32_e32 v108, 16, v23
	v_mul_f32_e32 v109, v109, v109
	v_fmac_f32_e32 v109, v108, v108
	v_mul_f32_e32 v79, v79, v208
	v_mul_f32_e32 v81, v81, v209
	v_cvt_pk_bf16_f32 v83, v79, v81
	v_mul_f32_e32 v79, v118, v110
	v_mul_f32_e32 v81, v118, v111
	v_and_b32_e32 v111, 0xffff0000, v24
	v_lshlrev_b32_e32 v110, 16, v24
	v_mul_f32_e32 v111, v111, v111
	v_fmac_f32_e32 v111, v110, v110
	v_mul_f32_e32 v79, v79, v210
	v_mul_f32_e32 v81, v81, v211
	v_cvt_pk_bf16_f32 v84, v79, v81
	v_mul_f32_e32 v79, v118, v112
	v_mul_f32_e32 v81, v118, v113
	v_and_b32_e32 v113, 0xffff0000, v25
	v_lshlrev_b32_e32 v112, 16, v25
	v_mul_f32_e32 v113, v113, v113
	v_fmac_f32_e32 v113, v112, v112
	v_mul_f32_e32 v79, v79, v212
	v_mul_f32_e32 v81, v81, v213
	v_cvt_pk_bf16_f32 v85, v79, v81
	global_store_dwordx4 v78, v[82:85], s[12:13] offset:32
	v_mul_f32_e32 v79, v118, v114
	v_mul_f32_e32 v81, v118, v115
	v_and_b32_e32 v115, 0xffff0000, v18
	v_lshlrev_b32_e32 v114, 16, v18
	v_mul_f32_e32 v115, v115, v115
	v_fmac_f32_e32 v115, v114, v114
	v_mul_f32_e32 v79, v79, v214
	v_mul_f32_e32 v81, v81, v215
	v_cvt_pk_bf16_f32 v82, v79, v81
	v_mul_f32_e32 v79, v118, v116
	v_mul_f32_e32 v81, v118, v117
	v_and_b32_e32 v117, 0xffff0000, v19
	v_lshlrev_b32_e32 v116, 16, v19
	v_mul_f32_e32 v117, v117, v117
	v_fmac_f32_e32 v117, v116, v116
	v_mul_f32_e32 v79, v79, v216
	v_mul_f32_e32 v81, v81, v217
	v_cvt_pk_bf16_f32 v83, v79, v81
	v_mul_f32_e32 v79, v118, v86
	v_mul_f32_e32 v81, v118, v88
	v_lshlrev_b32_e32 v86, 16, v47
	v_lshlrev_b32_e32 v88, 16, v48
	v_mul_f32_e32 v79, v79, v218
	v_mul_f32_e32 v81, v81, v219
	v_cvt_pk_bf16_f32 v84, v79, v81
	v_mul_f32_e32 v79, v118, v87
	v_mul_f32_e32 v81, v118, v89
	v_and_b32_e32 v87, 0xffff0000, v47
	v_and_b32_e32 v89, 0xffff0000, v48
	v_mul_f32_e32 v94, v89, v89
	v_fmac_f32_e32 v94, v88, v88
	v_lshlrev_b32_e32 v118, 16, v20
	v_fmac_f32_e32 v119, v118, v118
	v_mul_f32_e32 v79, v79, v220
	v_mul_f32_e32 v81, v81, v221
	v_cvt_pk_bf16_f32 v85, v79, v81
	global_store_dwordx4 v78, v[82:85], s[12:13] offset:48
	v_and_b32_e32 v81, 0xffff0000, v46
	v_lshlrev_b32_e32 v79, 16, v46
	v_mul_f32_e32 v84, v81, v81
	v_mul_f32_e32 v85, v87, v87
	v_and_b32_e32 v93, 0xffff0000, v49
	v_fmac_f32_e32 v84, v79, v79
	v_fmac_f32_e32 v85, v86, v86
	v_lshlrev_b32_e32 v92, 16, v49
	v_mul_f32_e32 v95, v93, v93
	v_add_f32_e32 v84, v84, v85
	v_fmac_f32_e32 v95, v92, v92
	v_add_f32_e32 v84, v94, v84
	v_add_f32_e32 v84, v95, v84
	s_nop 1
	v_add_f32_dpp v84, v84, v84 quad_perm:[1,0,3,2] row_mask:0xf bank_mask:0xf bound_ctrl:1
	s_nop 1
	v_add_f32_dpp v84, v84, v84 quad_perm:[2,3,0,1] row_mask:0xf bank_mask:0xf bound_ctrl:1
	s_nop 1
	v_add_f32_dpp v84, v84, v84 row_half_mirror row_mask:0xf bank_mask:0xf bound_ctrl:1
	s_nop 1
	v_add_f32_dpp v84, v84, v84 row_mirror row_mask:0xf bank_mask:0xf bound_ctrl:1
	v_fmamk_f32 v84, v84, 0x3c000000, v1
	v_mul_f32_e32 v85, 0x4f800000, v84
	v_cmp_gt_f32_e32 vcc, s17, v84
	s_nop 1
	v_cndmask_b32_e32 v84, v84, v85, vcc
	v_sqrt_f32_e32 v85, v84
	s_nop 0
	v_add_u32_e32 v94, -1, v85
	v_add_u32_e32 v95, 1, v85
	v_fma_f32 v96, -v94, v85, v84
	v_fma_f32 v97, -v95, v85, v84
	v_cmp_ge_f32_e64 s[0:1], 0, v96
	s_nop 1
	v_cndmask_b32_e64 v85, v85, v94, s[0:1]
	v_cmp_lt_f32_e64 s[0:1], 0, v97
	s_nop 1
	v_cndmask_b32_e64 v85, v85, v95, s[0:1]
	v_mul_f32_e32 v94, 0x37800000, v85
	v_cndmask_b32_e32 v85, v85, v94, vcc
	v_cmp_class_f32_e32 vcc, v84, v80
	s_nop 1
	v_cndmask_b32_e32 v84, v85, v84, vcc
	v_div_scale_f32 v85, s[0:1], v84, v84, 1.0
	v_rcp_f32_e32 v94, v85
	v_div_scale_f32 v95, vcc, 1.0, v84, 1.0
	v_fma_f32 v96, -v85, v94, 1.0
	v_fmac_f32_e32 v94, v96, v94
	v_mul_f32_e32 v96, v95, v94
	v_fma_f32 v97, -v85, v96, v95
	v_fmac_f32_e32 v96, v97, v94
	v_fma_f32 v85, -v85, v96, v95
	v_div_fmas_f32 v85, v85, v94, v96
	v_div_fixup_f32 v94, v85, v84, 1.0
	v_mul_f32_e32 v79, v94, v79
	v_mul_f32_e32 v81, v94, v81
	v_and_b32_e32 v96, 0xffff0000, v15
	v_lshlrev_b32_e32 v95, 16, v15
	v_mul_f32_e32 v96, v96, v96
	v_lshlrev_b32_e32 v97, 16, v16
	v_fmac_f32_e32 v96, v95, v95
	v_fmac_f32_e32 v98, v97, v97
	v_mul_f32_e32 v79, v222, v79
	v_mul_f32_e32 v81, v223, v81
	v_cvt_pk_bf16_f32 v82, v79, v81
	v_mul_f32_e32 v79, v94, v86
	v_mul_f32_e32 v81, v94, v87
	v_mul_f32_e32 v86, v94, v88
	v_mul_f32_e32 v87, v94, v89
	v_and_b32_e32 v88, 0xffff0000, v32
	v_mul_f32_e32 v122, v88, v88
	v_lshlrev_b32_e32 v89, 16, v33
	v_fmac_f32_e32 v105, v89, v89
	v_lshl_add_u64 v[88:89], s[12:13], 0, v[90:91]
	v_add_co_u32_e32 v88, vcc, s16, v88
	v_mul_f32_e32 v79, v224, v79
	v_mul_f32_e32 v81, v225, v81
	v_cvt_pk_bf16_f32 v83, v79, v81
	v_and_b32_e32 v81, 0xffff0000, v14
	v_lshlrev_b32_e32 v79, 16, v14
	v_mul_f32_e32 v81, v81, v81
	v_fmac_f32_e32 v81, v79, v79
	v_add_f32_e32 v79, v81, v96
	v_add_f32_e32 v79, v98, v79
	v_add_f32_e32 v79, v100, v79
	v_add_f32_e32 v79, v102, v79
	v_add_f32_e32 v79, v104, v79
	v_addc_co_u32_e32 v89, vcc, 0, v89, vcc
	v_mul_f32_e32 v84, v86, v226
	v_mul_f32_e32 v85, v87, v227
	v_cvt_pk_bf16_f32 v84, v84, v85
	v_lshlrev_b32_e32 v85, 16, v32
	v_fmac_f32_e32 v122, v85, v85
	v_add_f32_e32 v79, v122, v79
	v_add_f32_e32 v79, v105, v79
	v_add_f32_e32 v79, v107, v79
	v_add_f32_e32 v79, v109, v79
	v_add_f32_e32 v79, v111, v79
	v_add_f32_e32 v79, v113, v79
	v_add_f32_e32 v79, v115, v79
	v_add_f32_e32 v79, v117, v79
	v_add_f32_e32 v79, v119, v79
	v_add_f32_e32 v79, v121, v79
	v_mul_f32_e32 v85, v94, v92
	v_mul_f32_e32 v92, v94, v93
	v_add_f32_dpp v79, v79, v79 quad_perm:[1,0,3,2] row_mask:0xf bank_mask:0xf bound_ctrl:1
	v_mul_f32_e32 v85, v85, v228
	v_add_f32_dpp v79, v79, v79 quad_perm:[2,3,0,1] row_mask:0xf bank_mask:0xf bound_ctrl:1
	v_mul_f32_e32 v86, v92, v229
	v_cvt_pk_bf16_f32 v85, v85, v86
	global_store_dwordx4 v[88:89], v[82:85], off
	v_add_f32_dpp v79, v79, v79 row_half_mirror row_mask:0xf bank_mask:0xf bound_ctrl:1
	s_nop 1
	v_add_f32_dpp v79, v79, v79 row_mirror row_mask:0xf bank_mask:0xf bound_ctrl:1
	v_mov_b32_e32 v81, v79
	s_nop 1
	v_permlane16_swap_b32 v81, v79
	s_nop 0
	v_add_f32_e32 v79, v81, v79
	v_mov_b32_e32 v81, v79
	s_nop 1
	v_permlane32_swap_b32 v81, v79
	s_and_saveexec_b64 s[12:13], s[2:3]
	s_cbranch_execz .LBB0_1222
; __device__ __forceinline__ void qk_finish(Frame& F, int row, const QkRow& R) {
;     ...
;         ss = wave_sum(ss);
;         if (lane == 0) F.RS[row] = 1.0f / sqrtf(ss * (1.f / GMW) + EPS);
;     }
; __device__ __forceinline__ void qknorm_rows(Frame& F) {
;     ...
;     while (hasA) {
;         const int rb = row + F.NGW; const bool hasB = rb < M;
;         if (hasB) qk_load(F, rb, B);
;         qk_finish(F, row, A);
;         if (!hasB) break;
;         row = rb + F.NGW; hasA = row < M;
	v_add_f32_e32 v79, v81, v79
	v_fmamk_f32 v79, v79, 0x3a000000, v1
	v_mul_f32_e32 v81, 0x4f800000, v79
	v_cmp_gt_f32_e32 vcc, s17, v79
	s_ashr_i32 s9, s8, 31
	s_nop 0
	v_cndmask_b32_e32 v79, v79, v81, vcc
	v_sqrt_f32_e32 v81, v79
	s_nop 0
	v_add_u32_e32 v82, -1, v81
	v_fma_f32 v84, -v82, v81, v79
	v_add_u32_e32 v83, 1, v81
	v_cmp_ge_f32_e64 s[0:1], 0, v84
	s_nop 1
	v_cndmask_b32_e64 v82, v81, v82, s[0:1]
	v_fma_f32 v81, -v83, v81, v79
	v_cmp_lt_f32_e64 s[0:1], 0, v81
	s_nop 1
	v_cndmask_b32_e64 v81, v82, v83, s[0:1]
	v_mul_f32_e32 v82, 0x37800000, v81
	v_cndmask_b32_e32 v81, v81, v82, vcc
	v_cmp_class_f32_e32 vcc, v79, v80
	s_nop 1
	v_cndmask_b32_e32 v79, v81, v79, vcc
	v_div_scale_f32 v81, s[0:1], v79, v79, 1.0
	v_rcp_f32_e32 v82, v81
	s_lshl_b64 s[0:1], s[8:9], 2
	s_add_u32 s0, s26, s0
	s_addc_u32 s1, s27, s1
	v_fma_f32 v83, -v81, v82, 1.0
	v_fmac_f32_e32 v82, v83, v82
	v_div_scale_f32 v83, vcc, 1.0, v79, 1.0
	v_mul_f32_e32 v84, v83, v82
	v_fma_f32 v85, -v81, v84, v83
	v_fmac_f32_e32 v84, v85, v82
	v_fma_f32 v81, -v81, v84, v83
	v_div_fmas_f32 v81, v81, v82, v84
	v_div_fixup_f32 v79, v81, v79, 1.0
	global_store_dword v91, v79, s[0:1]
	s_or_b64 exec, exec, s[12:13]
	s_andn2_b64 vcc, exec, s[10:11]
	s_mov_b64 s[0:1], -1
	s_cbranch_vccnz .LBB0_1217
	s_branch .LBB0_1223

; #define GAS __attribute__((address_space(1)))
; __device__ __forceinline__ unsigned pk2(float lo, float hi) { return pg8::cvt_pk_bf16(lo, hi); }
; __device__ __forceinline__ float sum4(float v) { v += dpp_f<0xB1>(v); v += dpp_f<0x4E>(v); return v; }
; __device__ __forceinline__ void qk_load(Frame& F, int row, QkRow& R) {
;     const bf16* prow = F.PROJ + (size_t)row * PNP; const int lane = F.lane;
; #pragma unroll
;     for (int i = 0; i < 4; ++i) { R.q[i] = ((const GAS v4u*)(prow + PQ + 32 * lane))[i]; R.g[i] = ((const GAS v4u*)(prow + PGV + 32 * lane))[i]; }
;     R.k = *(const GAS v4u*)(prow + PK + 8 * lane);
; }
; __device__ __forceinline__ void qk_finish(Frame& F, int row, const QkRow& R) {
;     bf16* prow = F.PROJ + (size_t)row * PNP; const int lane = F.lane;
;     {
;         float ss = 0.f;
; #pragma unroll
;         for (int i = 0; i < 4; ++i)
; #pragma unroll
;             for (int j = 0; j < 4; ++j) { const float a = bflo(R.q[i][j]), c = bfhi(R.q[i][j]); ss += a * a + c * c; }
;         ss = sum4(ss);
;         const float r = QSCALE / sqrtf(ss * (1.f / HD) + EPS); const float* g = F.qng + 32 * (lane & 3);
; #pragma unroll
;         for (int i = 0; i < 4; ++i) { v4u o;
; #pragma unroll
;             for (int j = 0; j < 4; ++j) o[j] = pk2(bflo(R.q[i][j]) * r * g[8 * i + 2 * j], bfhi(R.q[i][j]) * r * g[8 * i + 2 * j + 1]);
;             ((GAS v4u*)(prow + PQ + 32 * lane))[i] = o; }
; __device__ __forceinline__ void qknorm_rows(Frame& F) {
;     ...
;         row = rb + F.NGW; hasA = row < M;
;         if (hasA) qk_load(F, row, A);
.LBB0_1223:
	s_add_i32 s0, s14, s8
	s_cmpk_gt_i32 s0, 0x1fff
	s_cbranch_scc1 .Lqk_noA
	s_mul_hi_i32 s1, s0, 0x8a00
	s_mul_i32 s0, s0, 0x8a00
	v_readlane_b32 s8, v248, 12
	v_readlane_b32 s9, v248, 13
	s_add_u32 s0, s8, s0
	s_addc_u32 s1, s9, s1
	v_mov_b32_e32 v79, v91
	v_lshl_add_u64 v[14:15], s[0:1], 0, v[78:79]
	v_lshl_add_u64 v[26:27], v[14:15], 0, s[4:5]
	v_add_co_u32_e32 v14, vcc, s15, v14
	global_load_dwordx4 v[2:5], v78, s[0:1] offset:48
	global_load_dwordx4 v[6:9], v78, s[0:1] offset:32
	global_load_dwordx4 v[10:13], v78, s[0:1] offset:16
	v_addc_co_u32_e32 v15, vcc, 0, v15, vcc
	global_load_dwordx4 v[14:17], v[14:15], off offset:2048
	s_nop 0
	global_load_dwordx4 v[18:21], v[26:27], off offset:48
	global_load_dwordx4 v[22:25], v[26:27], off offset:32
	global_load_dwordx4 v[30:33], v[26:27], off offset:16
	v_lshl_add_u64 v[26:27], s[0:1], 0, v[90:91]
	v_add_co_u32_e32 v46, vcc, 0x1000, v26
	s_nop 1
	v_addc_co_u32_e32 v47, vcc, 0, v27, vcc
	global_load_dwordx4 v[26:29], v78, s[0:1]
	s_nop 0
	global_load_dwordx4 v[46:49], v[46:47], off
	s_waitcnt vmcnt(9)
.LBB0_1225:
	v_and_b32_e32 v81, 0xffff0000, v66
	v_and_b32_e32 v93, 0xffff0000, v67
	v_lshlrev_b32_e32 v79, 16, v66
	v_mul_f32_e32 v82, v81, v81
	v_lshlrev_b32_e32 v92, 16, v67
	v_mul_f32_e32 v83, v93, v93
	v_fmac_f32_e32 v82, v79, v79
	v_fmac_f32_e32 v83, v92, v92
	v_and_b32_e32 v95, 0xffff0000, v68
	v_add_f32_e32 v82, v82, v83
	v_lshlrev_b32_e32 v94, 16, v68
	v_mul_f32_e32 v83, v95, v95
	v_fmac_f32_e32 v83, v94, v94
	v_and_b32_e32 v97, 0xffff0000, v69
	v_add_f32_e32 v82, v83, v82
	v_lshlrev_b32_e32 v96, 16, v69
	v_mul_f32_e32 v83, v97, v97
	v_fmac_f32_e32 v83, v96, v96
	v_and_b32_e32 v99, 0xffff0000, v42
	v_add_f32_e32 v82, v83, v82
	v_lshlrev_b32_e32 v98, 16, v42
	v_mul_f32_e32 v83, v99, v99
	v_fmac_f32_e32 v83, v98, v98
	v_and_b32_e32 v101, 0xffff0000, v43
	v_add_f32_e32 v82, v83, v82
	v_lshlrev_b32_e32 v100, 16, v43
	v_mul_f32_e32 v83, v101, v101
	v_fmac_f32_e32 v83, v100, v100
	v_and_b32_e32 v103, 0xffff0000, v44
	v_add_f32_e32 v82, v83, v82
	v_lshlrev_b32_e32 v102, 16, v44
	v_mul_f32_e32 v83, v103, v103
	v_fmac_f32_e32 v83, v102, v102
	v_add_f32_e32 v84, v83, v82
	v_and_b32_e32 v105, 0xffff0000, v45
	v_lshlrev_b32_e32 v104, 16, v45
	v_mul_f32_e32 v85, v105, v105
	v_fmac_f32_e32 v85, v104, v104
	v_and_b32_e32 v107, 0xffff0000, v38
	v_add_f32_e32 v84, v85, v84
	v_lshlrev_b32_e32 v106, 16, v38
	v_mul_f32_e32 v85, v107, v107
	v_fmac_f32_e32 v85, v106, v106
	v_and_b32_e32 v109, 0xffff0000, v39
	v_add_f32_e32 v84, v85, v84
	v_lshlrev_b32_e32 v108, 16, v39
	v_mul_f32_e32 v85, v109, v109
	v_fmac_f32_e32 v85, v108, v108
	v_and_b32_e32 v111, 0xffff0000, v40
	v_add_f32_e32 v84, v85, v84
	v_lshlrev_b32_e32 v110, 16, v40
	v_mul_f32_e32 v85, v111, v111
	v_fmac_f32_e32 v85, v110, v110
	v_and_b32_e32 v113, 0xffff0000, v41
	v_add_f32_e32 v84, v85, v84
	v_lshlrev_b32_e32 v112, 16, v41
	v_mul_f32_e32 v85, v113, v113
	v_fmac_f32_e32 v85, v112, v112
	v_and_b32_e32 v115, 0xffff0000, v34
	v_add_f32_e32 v84, v85, v84
	v_lshlrev_b32_e32 v114, 16, v34
	v_mul_f32_e32 v85, v115, v115
	v_fmac_f32_e32 v85, v114, v114
	v_and_b32_e32 v117, 0xffff0000, v35
	v_add_f32_e32 v84, v85, v84
	v_lshlrev_b32_e32 v116, 16, v35
	v_mul_f32_e32 v85, v117, v117
	v_fmac_f32_e32 v85, v116, v116
	v_and_b32_e32 v89, 0xffff0000, v37
	v_and_b32_e32 v88, 0xffff0000, v36
	v_add_f32_e32 v118, v85, v84
	v_lshlrev_b32_e32 v87, 16, v37
	v_lshlrev_b32_e32 v86, 16, v36
	v_pk_mul_f32 v[84:85], v[88:89], v[88:89]
	s_nop 0
	v_pk_fma_f32 v[84:85], v[86:87], v[86:87], v[84:85]
	s_nop 0
	v_add_f32_e32 v84, v84, v118
	v_add_f32_e32 v84, v85, v84
	s_nop 1
	v_add_f32_dpp v84, v84, v84 quad_perm:[1,0,3,2] row_mask:0xf bank_mask:0xf bound_ctrl:1
	s_nop 1
	v_add_f32_dpp v84, v84, v84 quad_perm:[2,3,0,1] row_mask:0xf bank_mask:0xf bound_ctrl:1
	v_fmamk_f32 v84, v84, 0x3c000000, v1
	v_mul_f32_e32 v85, 0x4f800000, v84
	v_cmp_gt_f32_e32 vcc, s17, v84
	s_nop 1
	v_cndmask_b32_e32 v84, v84, v85, vcc
	v_sqrt_f32_e32 v85, v84
	s_nop 0
	v_add_u32_e32 v118, -1, v85
	v_fma_f32 v119, -v118, v85, v84
	v_cmp_ge_f32_e64 s[0:1], 0, v119
	v_add_u32_e32 v119, 1, v85
	s_nop 0
	v_cndmask_b32_e64 v118, v85, v118, s[0:1]
	v_fma_f32 v85, -v119, v85, v84
	v_cmp_lt_f32_e64 s[0:1], 0, v85
	s_nop 1
	v_cndmask_b32_e64 v85, v118, v119, s[0:1]
	v_mul_f32_e32 v118, 0x37800000, v85
	v_cndmask_b32_e32 v85, v85, v118, vcc
	v_cmp_class_f32_e32 vcc, v84, v80
	s_nop 1
	v_cndmask_b32_e32 v84, v85, v84, vcc
	v_div_scale_f32 v85, s[0:1], v84, v84, s18
	v_rcp_f32_e32 v118, v85
	v_readlane_b32 s0, v248, 12
	v_readlane_b32 s1, v248, 13
	s_add_u32 s8, s0, s19
	v_fma_f32 v119, -v85, v118, 1.0
	v_fmac_f32_e32 v118, v119, v118
	v_div_scale_f32 v119, vcc, s18, v84, s18
	v_mul_f32_e32 v120, v119, v118
	v_fma_f32 v121, -v85, v120, v119
	v_fmac_f32_e32 v120, v121, v118
	v_fma_f32 v85, -v85, v120, v119
	v_div_fmas_f32 v85, v85, v118, v120
	v_div_fixup_f32 v118, v85, v84, s18
	v_mul_f32_e32 v79, v118, v79
	v_mul_f32_e32 v81, v118, v81
	v_mul_f32_e32 v79, v190, v79
	v_mul_f32_e32 v81, v191, v81
	v_cvt_pk_bf16_f32 v82, v79, v81
	v_mul_f32_e32 v79, v118, v92
	v_mul_f32_e32 v81, v118, v93
	s_addc_u32 s9, s1, s7
	v_and_b32_e32 v119, 0xffff0000, v56
	v_and_b32_e32 v121, 0xffff0000, v57
	v_mul_f32_e32 v119, v119, v119
	v_lshlrev_b32_e32 v120, 16, v57
	v_mul_f32_e32 v121, v121, v121
	v_fmac_f32_e32 v121, v120, v120
	v_mul_f32_e32 v79, v192, v79
	v_mul_f32_e32 v81, v193, v81
	v_cvt_pk_bf16_f32 v83, v79, v81
	v_mul_f32_e32 v79, v118, v94
	v_mul_f32_e32 v81, v118, v95
	v_mul_f32_e32 v79, v79, v194
	v_mul_f32_e32 v81, v81, v195
	v_cvt_pk_bf16_f32 v84, v79, v81
	v_mul_f32_e32 v79, v118, v96
	v_mul_f32_e32 v81, v118, v97
; #define GAS __attribute__((address_space(1)))
; __device__ __forceinline__ unsigned pk2(float lo, float hi) { return pg8::cvt_pk_bf16(lo, hi); }
; __device__ __forceinline__ float sum16(float v) { v = sum4(v); v += dpp_f<0x141>(v); v += dpp_f<0x140>(v); return v; }
; __device__ __forceinline__ void qk_finish(Frame& F, int row, const QkRow& R) {
;     ...
; #pragma unroll
;         for (int i = 0; i < 4; ++i) { v4u o;
; #pragma unroll
;             for (int j = 0; j < 4; ++j) o[j] = pk2(bflo(R.q[i][j]) * r * g[8 * i + 2 * j], bfhi(R.q[i][j]) * r * g[8 * i + 2 * j + 1]);
;             ((GAS v4u*)(prow + PQ + 32 * lane))[i] = o; }
;     }
;     {
;         float ss = 0.f;
; #pragma unroll
;         for (int j = 0; j < 4; ++j) { const float a = bflo(R.k[j]), c = bfhi(R.k[j]); ss += a * a + c * c; }
;         ss = sum16(ss);
;         const float r = 1.0f / sqrtf(ss * (1.f / HD) + EPS); const float* g = F.kng + 8 * (lane & 15); v4u o;
; #pragma unroll
;         for (int j = 0; j < 4; ++j) o[j] = pk2(bflo(R.k[j]) * r * g[2 * j], bfhi(R.k[j]) * r * g[2 * j + 1]);
;         *(GAS v4u*)(prow + PK + 8 * lane) = o;
	v_mul_f32_e32 v79, v79, v196
	v_mul_f32_e32 v81, v81, v197
	v_cvt_pk_bf16_f32 v85, v79, v81
	global_store_dwordx4 v78, v[82:85], s[8:9]
	v_mul_f32_e32 v79, v118, v98
	v_mul_f32_e32 v81, v118, v99
	v_and_b32_e32 v98, 0xffff0000, v52
	v_mul_f32_e32 v98, v98, v98
	v_lshlrev_b32_e32 v99, 16, v53
	v_mul_f32_e32 v79, v79, v198
	v_mul_f32_e32 v81, v81, v199
	v_cvt_pk_bf16_f32 v82, v79, v81
	v_mul_f32_e32 v79, v118, v100
	v_mul_f32_e32 v81, v118, v101
	v_and_b32_e32 v100, 0xffff0000, v53
	v_mul_f32_e32 v100, v100, v100
	v_lshlrev_b32_e32 v101, 16, v62
	v_fmac_f32_e32 v100, v99, v99
	v_mul_f32_e32 v79, v79, v200
	v_mul_f32_e32 v81, v81, v201
	v_cvt_pk_bf16_f32 v83, v79, v81
	v_mul_f32_e32 v79, v118, v102
	v_mul_f32_e32 v81, v118, v103
	v_and_b32_e32 v102, 0xffff0000, v62
	v_mul_f32_e32 v102, v102, v102
	v_lshlrev_b32_e32 v103, 16, v63
	v_fmac_f32_e32 v102, v101, v101
	v_mul_f32_e32 v79, v79, v202
	v_mul_f32_e32 v81, v81, v203
	v_cvt_pk_bf16_f32 v84, v79, v81
	v_mul_f32_e32 v79, v118, v104
	v_mul_f32_e32 v81, v118, v105
	v_and_b32_e32 v104, 0xffff0000, v63
	v_mul_f32_e32 v104, v104, v104
	v_fmac_f32_e32 v104, v103, v103
	v_lshlrev_b32_e32 v105, 16, v65
	v_mul_f32_e32 v79, v79, v204
	v_mul_f32_e32 v81, v81, v205
	v_cvt_pk_bf16_f32 v85, v79, v81
	global_store_dwordx4 v78, v[82:85], s[8:9] offset:16
	v_mul_f32_e32 v79, v118, v106
	v_mul_f32_e32 v81, v118, v107
	v_and_b32_e32 v107, 0xffff0000, v58
	v_lshlrev_b32_e32 v106, 16, v58
	v_mul_f32_e32 v107, v107, v107
	v_fmac_f32_e32 v107, v106, v106
	v_mul_f32_e32 v79, v79, v206
	v_mul_f32_e32 v81, v81, v207
	v_cvt_pk_bf16_f32 v82, v79, v81
	v_mul_f32_e32 v79, v118, v108
	v_mul_f32_e32 v81, v118, v109
	v_and_b32_e32 v109, 0xffff0000, v59
	v_lshlrev_b32_e32 v108, 16, v59
	v_mul_f32_e32 v109, v109, v109
	v_fmac_f32_e32 v109, v108, v108
	v_mul_f32_e32 v79, v79, v208
	v_mul_f32_e32 v81, v81, v209
	v_cvt_pk_bf16_f32 v83, v79, v81
	v_mul_f32_e32 v79, v118, v110
	v_mul_f32_e32 v81, v118, v111
	v_and_b32_e32 v111, 0xffff0000, v60
	v_lshlrev_b32_e32 v110, 16, v60
	v_mul_f32_e32 v111, v111, v111
	v_fmac_f32_e32 v111, v110, v110
	v_mul_f32_e32 v79, v79, v210
	v_mul_f32_e32 v81, v81, v211
	v_cvt_pk_bf16_f32 v84, v79, v81
	v_mul_f32_e32 v79, v118, v112
	v_mul_f32_e32 v81, v118, v113
	v_and_b32_e32 v113, 0xffff0000, v61
	v_lshlrev_b32_e32 v112, 16, v61
	v_mul_f32_e32 v113, v113, v113
	v_fmac_f32_e32 v113, v112, v112
	v_mul_f32_e32 v79, v79, v212
	v_mul_f32_e32 v81, v81, v213
	v_cvt_pk_bf16_f32 v85, v79, v81
	global_store_dwordx4 v78, v[82:85], s[8:9] offset:32
	v_mul_f32_e32 v79, v118, v114
	v_mul_f32_e32 v81, v118, v115
	v_and_b32_e32 v115, 0xffff0000, v54
	v_lshlrev_b32_e32 v114, 16, v54
	v_mul_f32_e32 v115, v115, v115
	v_fmac_f32_e32 v115, v114, v114
	v_mul_f32_e32 v79, v79, v214
	v_mul_f32_e32 v81, v81, v215
	v_cvt_pk_bf16_f32 v82, v79, v81
	v_mul_f32_e32 v79, v118, v116
	v_mul_f32_e32 v81, v118, v117
	v_and_b32_e32 v117, 0xffff0000, v55
	v_lshlrev_b32_e32 v116, 16, v55
	v_mul_f32_e32 v117, v117, v117
	v_fmac_f32_e32 v117, v116, v116
	v_mul_f32_e32 v79, v79, v216
	v_mul_f32_e32 v81, v81, v217
	v_cvt_pk_bf16_f32 v83, v79, v81
	v_mul_f32_e32 v79, v118, v86
	v_mul_f32_e32 v81, v118, v88
	v_lshlrev_b32_e32 v86, 16, v71
	v_lshlrev_b32_e32 v88, 16, v72
	v_mul_f32_e32 v79, v79, v218
	v_mul_f32_e32 v81, v81, v219
	v_cvt_pk_bf16_f32 v84, v79, v81
	v_mul_f32_e32 v79, v118, v87
	v_mul_f32_e32 v81, v118, v89
	v_and_b32_e32 v87, 0xffff0000, v71
	v_and_b32_e32 v89, 0xffff0000, v72
	v_mul_f32_e32 v94, v89, v89
	v_fmac_f32_e32 v94, v88, v88
	v_lshlrev_b32_e32 v118, 16, v56
	v_fmac_f32_e32 v119, v118, v118
	v_mul_f32_e32 v79, v79, v220
	v_mul_f32_e32 v81, v81, v221
	v_cvt_pk_bf16_f32 v85, v79, v81
	global_store_dwordx4 v78, v[82:85], s[8:9] offset:48
	v_and_b32_e32 v81, 0xffff0000, v70
	v_lshlrev_b32_e32 v79, 16, v70
	v_mul_f32_e32 v84, v81, v81
	v_mul_f32_e32 v85, v87, v87
	v_and_b32_e32 v93, 0xffff0000, v73
	v_fmac_f32_e32 v84, v79, v79
	v_fmac_f32_e32 v85, v86, v86
	v_lshlrev_b32_e32 v92, 16, v73
	v_mul_f32_e32 v95, v93, v93
	v_add_f32_e32 v84, v84, v85
	v_fmac_f32_e32 v95, v92, v92
	v_add_f32_e32 v84, v94, v84
	v_add_f32_e32 v84, v95, v84
	s_nop 1
	v_add_f32_dpp v84, v84, v84 quad_perm:[1,0,3,2] row_mask:0xf bank_mask:0xf bound_ctrl:1
	s_nop 1
	v_add_f32_dpp v84, v84, v84 quad_perm:[2,3,0,1] row_mask:0xf bank_mask:0xf bound_ctrl:1
	s_nop 1
	v_add_f32_dpp v84, v84, v84 row_half_mirror row_mask:0xf bank_mask:0xf bound_ctrl:1
	s_nop 1
	v_add_f32_dpp v84, v84, v84 row_mirror row_mask:0xf bank_mask:0xf bound_ctrl:1
	v_fmamk_f32 v84, v84, 0x3c000000, v1
; #define GAS __attribute__((address_space(1)))
; __device__ __forceinline__ unsigned pk2(float lo, float hi) { return pg8::cvt_pk_bf16(lo, hi); }
; __device__ __forceinline__ float sum16(float v) { v = sum4(v); v += dpp_f<0x141>(v); v += dpp_f<0x140>(v); return v; }
; __device__ __forceinline__ void qk_finish(Frame& F, int row, const QkRow& R) {
;     ...
;     {
;         float ss = 0.f;
; #pragma unroll
;         for (int j = 0; j < 4; ++j) { const float a = bflo(R.k[j]), c = bfhi(R.k[j]); ss += a * a + c * c; }
;         ss = sum16(ss);
;         const float r = 1.0f / sqrtf(ss * (1.f / HD) + EPS); const float* g = F.kng + 8 * (lane & 15); v4u o;
; #pragma unroll
;         for (int j = 0; j < 4; ++j) o[j] = pk2(bflo(R.k[j]) * r * g[2 * j], bfhi(R.k[j]) * r * g[2 * j + 1]);
;         *(GAS v4u*)(prow + PK + 8 * lane) = o;
;     }
;     {
;         float ss = 0.f;
; #pragma unroll
;         for (int i = 0; i < 4; ++i)
; #pragma unroll
;             for (int j = 0; j < 4; ++j) { const float a = bflo(R.g[i][j]), c = bfhi(R.g[i][j]); ss += a * a + c * c; }
;         ss = wave_sum(ss);
;         if (lane == 0) F.RS[row] = 1.0f / sqrtf(ss * (1.f / GMW) + EPS);
;     }
	v_mul_f32_e32 v85, 0x4f800000, v84
	v_cmp_gt_f32_e32 vcc, s17, v84
	s_nop 1
	v_cndmask_b32_e32 v84, v84, v85, vcc
	v_sqrt_f32_e32 v85, v84
	s_nop 0
	v_add_u32_e32 v94, -1, v85
	v_add_u32_e32 v95, 1, v85
	v_fma_f32 v96, -v94, v85, v84
	v_fma_f32 v97, -v95, v85, v84
	v_cmp_ge_f32_e64 s[0:1], 0, v96
	s_nop 1
	v_cndmask_b32_e64 v85, v85, v94, s[0:1]
	v_cmp_lt_f32_e64 s[0:1], 0, v97
	s_nop 1
	v_cndmask_b32_e64 v85, v85, v95, s[0:1]
	v_mul_f32_e32 v94, 0x37800000, v85
	v_cndmask_b32_e32 v85, v85, v94, vcc
	v_cmp_class_f32_e32 vcc, v84, v80
	s_nop 1
	v_cndmask_b32_e32 v84, v85, v84, vcc
	v_div_scale_f32 v85, s[0:1], v84, v84, 1.0
	v_rcp_f32_e32 v94, v85
	v_div_scale_f32 v95, vcc, 1.0, v84, 1.0
	v_fma_f32 v96, -v85, v94, 1.0
	v_fmac_f32_e32 v94, v96, v94
	v_mul_f32_e32 v96, v95, v94
	v_fma_f32 v97, -v85, v96, v95
	v_fmac_f32_e32 v96, v97, v94
	v_fma_f32 v85, -v85, v96, v95
	v_div_fmas_f32 v85, v85, v94, v96
	v_div_fixup_f32 v94, v85, v84, 1.0
	v_mul_f32_e32 v79, v94, v79
	v_mul_f32_e32 v81, v94, v81
	v_and_b32_e32 v96, 0xffff0000, v51
	v_lshlrev_b32_e32 v95, 16, v51
	v_mul_f32_e32 v96, v96, v96
	v_lshlrev_b32_e32 v97, 16, v52
	v_fmac_f32_e32 v96, v95, v95
	v_fmac_f32_e32 v98, v97, v97
	v_mul_f32_e32 v79, v222, v79
	v_mul_f32_e32 v81, v223, v81
	v_cvt_pk_bf16_f32 v82, v79, v81
	v_mul_f32_e32 v79, v94, v86
	v_mul_f32_e32 v81, v94, v87
	v_mul_f32_e32 v86, v94, v88
	v_mul_f32_e32 v87, v94, v89
	v_and_b32_e32 v88, 0xffff0000, v64
	v_and_b32_e32 v89, 0xffff0000, v65
	v_mul_f32_e32 v122, v88, v88
	v_mul_f32_e32 v123, v89, v89
	v_fmac_f32_e32 v123, v105, v105
	v_lshl_add_u64 v[88:89], s[8:9], 0, v[90:91]
	v_add_co_u32_e32 v88, vcc, s16, v88
	v_mul_f32_e32 v79, v224, v79
	v_mul_f32_e32 v81, v225, v81
	v_cvt_pk_bf16_f32 v83, v79, v81
	v_and_b32_e32 v81, 0xffff0000, v50
	v_lshlrev_b32_e32 v79, 16, v50
	v_mul_f32_e32 v81, v81, v81
	v_fmac_f32_e32 v81, v79, v79
	v_add_f32_e32 v79, v81, v96
	v_add_f32_e32 v79, v98, v79
	v_add_f32_e32 v79, v100, v79
	v_add_f32_e32 v79, v102, v79
	v_add_f32_e32 v79, v104, v79
	v_addc_co_u32_e32 v89, vcc, 0, v89, vcc
	v_mul_f32_e32 v84, v86, v226
	v_mul_f32_e32 v85, v87, v227
	v_cvt_pk_bf16_f32 v84, v84, v85
	v_lshlrev_b32_e32 v85, 16, v64
	v_fmac_f32_e32 v122, v85, v85
	v_add_f32_e32 v79, v122, v79
	v_add_f32_e32 v79, v123, v79
	v_add_f32_e32 v79, v107, v79
	v_add_f32_e32 v79, v109, v79
	v_add_f32_e32 v79, v111, v79
	v_add_f32_e32 v79, v113, v79
	v_add_f32_e32 v79, v115, v79
	v_add_f32_e32 v79, v117, v79
	v_add_f32_e32 v79, v119, v79
	v_add_f32_e32 v79, v121, v79
	v_mul_f32_e32 v85, v94, v92
	v_mul_f32_e32 v92, v94, v93
	v_add_f32_dpp v79, v79, v79 quad_perm:[1,0,3,2] row_mask:0xf bank_mask:0xf bound_ctrl:1
	v_mul_f32_e32 v85, v85, v228
	v_add_f32_dpp v79, v79, v79 quad_perm:[2,3,0,1] row_mask:0xf bank_mask:0xf bound_ctrl:1
	v_mul_f32_e32 v86, v92, v229
	v_cvt_pk_bf16_f32 v85, v85, v86
	global_store_dwordx4 v[88:89], v[82:85], off
	v_add_f32_dpp v79, v79, v79 row_half_mirror row_mask:0xf bank_mask:0xf bound_ctrl:1
	s_nop 1
	v_add_f32_dpp v79, v79, v79 row_mirror row_mask:0xf bank_mask:0xf bound_ctrl:1
	v_mov_b32_e32 v81, v79
	s_nop 1
	v_permlane16_swap_b32 v79, v81
	s_nop 0
	v_add_f32_e32 v79, v79, v81
	v_mov_b32_e32 v81, v79
	s_nop 1
	v_permlane32_swap_b32 v79, v81
	s_and_saveexec_b64 s[8:9], s[2:3]
	s_cbranch_execz .LBB0_1216
	v_add_f32_e32 v79, v79, v81
	v_fmamk_f32 v79, v79, 0x3a000000, v1
	v_mul_f32_e32 v81, 0x4f800000, v79
	v_cmp_gt_f32_e32 vcc, s17, v79
	s_ashr_i32 s7, s6, 31
	s_nop 0
	v_cndmask_b32_e32 v79, v79, v81, vcc
	v_sqrt_f32_e32 v81, v79
	s_nop 0
	v_add_u32_e32 v82, -1, v81
	v_fma_f32 v84, -v82, v81, v79
	v_add_u32_e32 v83, 1, v81
	v_cmp_ge_f32_e64 s[0:1], 0, v84
	s_nop 1
	v_cndmask_b32_e64 v82, v81, v82, s[0:1]
	v_fma_f32 v81, -v83, v81, v79
	v_cmp_lt_f32_e64 s[0:1], 0, v81
	s_nop 1
	v_cndmask_b32_e64 v81, v82, v83, s[0:1]
	v_mul_f32_e32 v82, 0x37800000, v81
	v_cndmask_b32_e32 v81, v81, v82, vcc
	v_cmp_class_f32_e32 vcc, v79, v80
	s_nop 1
	v_cndmask_b32_e32 v79, v81, v79, vcc
	v_div_scale_f32 v81, s[0:1], v79, v79, 1.0
	v_rcp_f32_e32 v82, v81
	s_lshl_b64 s[0:1], s[6:7], 2
	s_add_u32 s0, s26, s0
	s_addc_u32 s1, s27, s1
	v_fma_f32 v83, -v81, v82, 1.0
	v_fmac_f32_e32 v82, v83, v82
	v_div_scale_f32 v83, vcc, 1.0, v79, 1.0
	v_mul_f32_e32 v84, v83, v82
	v_fma_f32 v85, -v81, v84, v83
	v_fmac_f32_e32 v84, v85, v82
	v_fma_f32 v81, -v81, v84, v83
	v_div_fmas_f32 v81, v81, v82, v84
	v_div_fixup_f32 v79, v81, v79, 1.0
	global_store_dword v91, v79, s[0:1]
	s_branch .LBB0_1216
.Lqk_noB:
	s_waitcnt vmcnt(0)
	s_branch .LBB0_1220
